# speedup vs baseline: 1.0285x; 1.0285x over previous
.LBB0_3:
	v_lshl_or_b32 v2, s2, 8, v0
	s_load_dwordx2 s[4:5], s[0:1], 0x30
	s_load_dwordx2 s[6:7], s[0:1], 0x50
	v_add_u32_e32 v2, 0xfffd0000, v2
	v_lshrrev_b32_e32 v3, 4, v2
	v_and_b32_e32 v4, 8, v1
	s_mov_b32 s3, 0xffffff0
	v_and_or_b32 v4, v3, s3, v4
	v_mov_b32_e32 v5, 0
	v_lshlrev_b64 v[6:7], 9, v[4:5]
	v_lshlrev_b32_e32 v3, 1, v0
	s_waitcnt lgkmcnt(0)
	v_lshl_add_u64 v[6:7], s[4:5], 0, v[6:7]
	v_and_b32_e32 v4, 0x180, v3
	v_and_b32_e32 v3, 31, v0
	v_lshl_add_u64 v[6:7], v[6:7], 0, v[4:5]
	v_lshlrev_b32_e32 v4, 2, v3
	v_lshl_add_u64 v[6:7], v[6:7], 0, v[4:5]
	global_load_dword v8, v[6:7], off offset:1024
	global_load_dword v9, v[6:7], off offset:1536
	global_load_dword v4, v[6:7], off offset:2048
	global_load_dword v10, v[6:7], off offset:3072
	global_load_dword v11, v[6:7], off offset:3584
	global_load_dword v12, v[6:7], off offset:2560
	global_load_dword v13, v[6:7], off
	global_load_dword v14, v[6:7], off offset:512
	v_mov_b32_e32 v3, v5
	v_lshl_add_u64 v[6:7], v[2:3], 4, s[6:7]
	s_waitcnt vmcnt(6)
	v_cvt_pk_f16_f32 v3, v8, v9
	s_waitcnt vmcnt(3)
	v_cvt_pk_f16_f32 v5, v10, v11
	s_waitcnt vmcnt(2)
	v_cvt_pk_f16_f32 v4, v4, v12
	s_waitcnt vmcnt(0)
	v_cvt_pk_f16_f32 v2, v13, v14
	global_store_dwordx4 v[6:7], v[2:5], off sc1
	s_cbranch_execnz .LBB0_2
.LBB0_4:
	s_load_dwordx4 s[8:11], s[0:1], 0x18
	s_load_dwordx2 s[6:7], s[0:1], 0x28
	s_ashr_i32 s4, s2, 8
	s_cmp_eq_u32 s4, 1
	v_mov_b32_e32 v19, 0
	v_lshlrev_b32_e32 v4, 6, v0
	s_waitcnt lgkmcnt(0)
	s_cselect_b32 s3, s10, s6
	s_cselect_b32 s5, s11, s7
	s_cmpk_lt_u32 s2, 0x100
	s_cselect_b32 s7, s9, s5
	s_cselect_b32 s6, s8, s3
	s_lshl_b32 s3, s2, 2
	s_and_b32 s8, s3, 0x3c0
	s_lshl_b32 s2, s2, 6
	v_or_b32_e32 v2, s8, v1
	s_and_b32 s9, s2, 0x3c0
	v_lshlrev_b32_e32 v18, 12, v2
	s_mov_b32 s3, 0
	v_lshl_add_u64 v[2:3], s[6:7], 0, v[18:19]
	s_lshl_b32 s2, s9, 2
	v_lshl_add_u64 v[2:3], v[2:3], 0, s[2:3]
	v_and_b32_e32 v18, 0xc0, v4
	v_lshl_add_u64 v[20:21], v[2:3], 0, v[18:19]
	global_load_dwordx4 v[2:5], v[20:21], off
	global_load_dwordx4 v[6:9], v[20:21], off offset:16
	global_load_dwordx4 v[10:13], v[20:21], off offset:32
	global_load_dwordx4 v[14:17], v[20:21], off offset:48
	v_and_b32_e32 v20, 7, v0
	v_lshrrev_b32_e32 v21, 3, v0
	v_or_b32_e32 v0, 0x100, v0
	s_load_dwordx2 s[0:1], s[0:1], 0x48
	s_movk_i32 s6, 0x104
	s_movk_i32 s2, 0x820
	v_lshlrev_b32_e32 v22, 2, v21
	v_lshrrev_b32_e32 v0, 3, v0
	v_mad_u32_u24 v24, v20, s2, v22
	v_lshlrev_b32_e32 v22, 2, v0
	v_or_b32_e32 v28, s9, v0
	v_mad_u32_u24 v0, v1, s6, v18
	v_add_u32_e32 v25, 0x400, v24
	s_ashr_i32 s5, s4, 31
	v_mad_u32_u24 v26, v20, s2, v22
	s_lshl_b64 s[2:3], s[4:5], 21
	s_waitcnt lgkmcnt(0)
	s_add_u32 s0, s0, s2
	s_addc_u32 s1, s1, s3
	s_lshl_b32 s2, s8, 1
	v_add_u32_e32 v27, 0x400, v26
	s_add_u32 s0, s0, s2
	v_or_b32_e32 v22, s9, v21
	s_addc_u32 s1, s1, 0
	v_lshlrev_b32_e32 v18, 4, v20
	v_lshl_add_u64 v[20:21], s[0:1], 0, v[18:19]
	v_lshlrev_b32_e32 v18, 11, v22
	v_lshl_add_u64 v[22:23], v[20:21], 0, v[18:19]
	v_lshlrev_b32_e32 v18, 11, v28
	s_waitcnt vmcnt(3)
	ds_write2_b32 v0, v2, v3 offset1:1
	ds_write2_b32 v0, v4, v5 offset0:2 offset1:3
	s_waitcnt vmcnt(2)
	ds_write2_b32 v0, v6, v7 offset0:4 offset1:5
	ds_write2_b32 v0, v8, v9 offset0:6 offset1:7
	s_waitcnt vmcnt(1)
	ds_write2_b32 v0, v10, v11 offset0:8 offset1:9
	ds_write2_b32 v0, v12, v13 offset0:10 offset1:11
	s_waitcnt vmcnt(0)
	ds_write2_b32 v0, v14, v15 offset0:12 offset1:13
	ds_write2_b32 v0, v16, v17 offset0:14 offset1:15
	s_waitcnt lgkmcnt(0)
	s_barrier
	ds_read2_b32 v[0:1], v24 offset1:65
	ds_read2_b32 v[2:3], v24 offset0:130 offset1:195
	ds_read2_b32 v[4:5], v25 offset0:4 offset1:69
	ds_read2_b32 v[6:7], v25 offset0:134 offset1:199
	s_waitcnt lgkmcnt(3)
	v_cvt_pk_bf16_f32 v0, v0, v1
	s_waitcnt lgkmcnt(2)
	v_cvt_pk_bf16_f32 v1, v2, v3
	s_waitcnt lgkmcnt(1)
	v_cvt_pk_bf16_f32 v2, v4, v5
	s_waitcnt lgkmcnt(0)
	v_cvt_pk_bf16_f32 v3, v6, v7
	ds_read2_b32 v[4:5], v26 offset1:65
	ds_read2_b32 v[6:7], v26 offset0:130 offset1:195
	ds_read2_b32 v[8:9], v27 offset0:4 offset1:69
	ds_read2_b32 v[10:11], v27 offset0:134 offset1:199
	global_store_dwordx4 v[22:23], v[0:3], off sc1
	s_waitcnt lgkmcnt(3)
	s_nop 0
	v_cvt_pk_bf16_f32 v0, v4, v5
	v_lshl_add_u64 v[4:5], v[20:21], 0, v[18:19]
	s_waitcnt lgkmcnt(2)
	v_cvt_pk_bf16_f32 v1, v6, v7
	s_waitcnt lgkmcnt(1)
	v_cvt_pk_bf16_f32 v2, v8, v9
	s_waitcnt lgkmcnt(0)
	v_cvt_pk_bf16_f32 v3, v10, v11
	global_store_dwordx4 v[4:5], v[0:3], off sc1
	s_endpgm

.LBB1_1:
	s_and_b32 s0, s29, 0x10000
	v_add_u32_e32 v211, s0, v209
	v_add_u32_e32 v242, s0, v210
	ds_read_b128 v[212:215], v242 offset:0
	ds_read_b128 v[216:219], v242 offset:0x800
	ds_read_b128 v[220:223], v242 offset:0x1000
	ds_read_b128 v[224:227], v242 offset:0x1800
	ds_read_b128 v[228:231], v211 offset:0
	ds_read_b128 v[232:235], v211 offset:0x800
	ds_read_b128 v[236:239], v211 offset:0x1000
	s_nop 0
	s_waitcnt lgkmcnt(2)
	s_nop 0
	v_mfma_f32_16x16x32_bf16 v[174:177], v[212:215], v[228:231], v[174:177]
	v_mfma_f32_16x16x32_bf16 v[170:173], v[216:219], v[228:231], v[170:173]
	v_mfma_f32_16x16x32_bf16 v[166:169], v[220:223], v[228:231], v[166:169]
	v_mfma_f32_16x16x32_bf16 v[162:165], v[224:227], v[228:231], v[162:165]
	ds_read_b128 v[228:231], v211 offset:0x1800
	s_waitcnt lgkmcnt(2)
	s_nop 0
	v_mfma_f32_16x16x32_bf16 v[158:161], v[212:215], v[232:235], v[158:161]
	v_mfma_f32_16x16x32_bf16 v[154:157], v[216:219], v[232:235], v[154:157]
	v_mfma_f32_16x16x32_bf16 v[150:153], v[220:223], v[232:235], v[150:153]
	v_mfma_f32_16x16x32_bf16 v[146:149], v[224:227], v[232:235], v[146:149]
	ds_read_b128 v[232:235], v211 offset:0x2000
	s_waitcnt lgkmcnt(2)
	s_nop 0
	v_mfma_f32_16x16x32_bf16 v[142:145], v[212:215], v[236:239], v[142:145]
	v_mfma_f32_16x16x32_bf16 v[138:141], v[216:219], v[236:239], v[138:141]
	v_mfma_f32_16x16x32_bf16 v[134:137], v[220:223], v[236:239], v[134:137]
	v_mfma_f32_16x16x32_bf16 v[130:133], v[224:227], v[236:239], v[130:133]
	ds_read_b128 v[236:239], v211 offset:0x2800
	s_waitcnt lgkmcnt(2)
	s_nop 0
	v_mfma_f32_16x16x32_bf16 v[126:129], v[212:215], v[228:231], v[126:129]
	v_mfma_f32_16x16x32_bf16 v[122:125], v[216:219], v[228:231], v[122:125]
	v_mfma_f32_16x16x32_bf16 v[118:121], v[220:223], v[228:231], v[118:121]
	v_mfma_f32_16x16x32_bf16 v[114:117], v[224:227], v[228:231], v[114:117]
	ds_read_b128 v[228:231], v211 offset:0x3000
	s_waitcnt lgkmcnt(2)
	s_nop 0
	v_mfma_f32_16x16x32_bf16 v[110:113], v[212:215], v[232:235], v[110:113]
	v_mfma_f32_16x16x32_bf16 v[106:109], v[216:219], v[232:235], v[106:109]
	v_mfma_f32_16x16x32_bf16 v[102:105], v[220:223], v[232:235], v[102:105]
	v_mfma_f32_16x16x32_bf16 v[98:101], v[224:227], v[232:235], v[98:101]
	ds_read_b128 v[232:235], v211 offset:0x3800
	s_waitcnt lgkmcnt(2)
	s_nop 0
	v_mfma_f32_16x16x32_bf16 v[94:97], v[212:215], v[236:239], v[94:97]
	v_mfma_f32_16x16x32_bf16 v[90:93], v[216:219], v[236:239], v[90:93]
	v_mfma_f32_16x16x32_bf16 v[86:89], v[220:223], v[236:239], v[86:89]
	v_mfma_f32_16x16x32_bf16 v[82:85], v[224:227], v[236:239], v[82:85]
	s_waitcnt lgkmcnt(1)
	s_nop 0
	v_mfma_f32_16x16x32_bf16 v[78:81], v[212:215], v[228:231], v[78:81]
	v_mfma_f32_16x16x32_bf16 v[74:77], v[216:219], v[228:231], v[74:77]
	v_mfma_f32_16x16x32_bf16 v[70:73], v[220:223], v[228:231], v[70:73]
	v_mfma_f32_16x16x32_bf16 v[66:69], v[224:227], v[228:231], v[66:69]
	s_waitcnt lgkmcnt(0)
	s_nop 0
	v_mfma_f32_16x16x32_bf16 v[62:65], v[212:215], v[232:235], v[62:65]
	v_mfma_f32_16x16x32_bf16 v[58:61], v[216:219], v[232:235], v[58:61]
	v_mfma_f32_16x16x32_bf16 v[54:57], v[220:223], v[232:235], v[54:57]
	v_mfma_f32_16x16x32_bf16 v[50:53], v[224:227], v[232:235], v[50:53]
	s_xor_b32 s0, s0, 0x10000
	s_and_b32 s1, s22, 0x3c0
	s_add_i32 s23, s0, 0
	s_lshl_b32 s0, s1, 2
	s_add_u32 s20, s25, s0
	s_waitcnt vmcnt(10)
	v_cvt_pk_bf16_f32 v46, v46, v47
	v_cvt_pk_bf16_f32 v47, v48, v49
	v_cvt_pk_bf16_f32 v48, v42, v43
	v_cvt_pk_bf16_f32 v49, v44, v45
	s_waitcnt vmcnt(8)
	v_cvt_pk_bf16_f32 v38, v38, v39
	v_cvt_pk_bf16_f32 v39, v40, v41
	v_cvt_pk_bf16_f32 v40, v34, v35
	v_add_u32_e32 v34, s23, v208
	s_addc_u32 s21, s26, 0
	s_lshl_b32 s0, s1, 1
	v_cvt_pk_bf16_f32 v41, v36, v37
	v_lshlrev_b32_e32 v182, 2, v178
	v_add_u32_e32 v35, s23, v205
	v_add_u32_e32 v36, s23, v206
	v_add_u32_e32 v37, s23, v207
	ds_write_b128 v34, v[46:49]
	ds_write_b128 v35, v[38:41]
	s_waitcnt vmcnt(7)
	ds_write_b128 v36, v[30:33] offset:32768
	s_waitcnt vmcnt(6)
	ds_write_b128 v37, v[26:29] offset:32768
	v_lshl_add_u64 v[26:27], s[20:21], 0, v[180:181]
	v_lshl_add_u64 v[28:29], s[20:21], 0, v[184:185]
	s_add_u32 s0, s27, s0
	v_lshl_add_u64 v[26:27], v[26:27], 0, v[182:183]
	v_lshl_add_u64 v[28:29], v[28:29], 0, v[182:183]
	s_addc_u32 s1, s28, 0
	v_lshlrev_b32_e32 v240, 1, v178
	v_mov_b32_e32 v241, v183
	global_load_dwordx4 v[42:45], v[26:27], off offset:16
	global_load_dwordx4 v[46:49], v[26:27], off
	global_load_dwordx4 v[34:37], v[28:29], off offset:16
	global_load_dwordx4 v[38:41], v[28:29], off
	v_lshl_add_u64 v[26:27], s[0:1], 0, v[186:187]
	v_lshl_add_u64 v[28:29], s[0:1], 0, v[188:189]
	v_lshl_add_u64 v[26:27], v[26:27], 0, v[240:241]
	v_lshl_add_u64 v[28:29], v[28:29], 0, v[240:241]
	global_load_dwordx4 v[30:33], v[26:27], off
	s_nop 0
	global_load_dwordx4 v[26:29], v[28:29], off
	ds_read_b128 v[212:215], v242 offset:0x400
	ds_read_b128 v[216:219], v242 offset:0xc00
	ds_read_b128 v[220:223], v242 offset:0x1400
	ds_read_b128 v[224:227], v242 offset:0x1c00
	ds_read_b128 v[228:231], v211 offset:0x400
	ds_read_b128 v[232:235], v211 offset:0xc00
	ds_read_b128 v[236:239], v211 offset:0x1400
	s_nop 0
	s_waitcnt lgkmcnt(2)
	s_nop 0
	v_mfma_f32_16x16x32_bf16 v[174:177], v[212:215], v[228:231], v[174:177]
	v_mfma_f32_16x16x32_bf16 v[170:173], v[216:219], v[228:231], v[170:173]
	v_mfma_f32_16x16x32_bf16 v[166:169], v[220:223], v[228:231], v[166:169]
	v_mfma_f32_16x16x32_bf16 v[162:165], v[224:227], v[228:231], v[162:165]
	ds_read_b128 v[228:231], v211 offset:0x1c00
	s_waitcnt lgkmcnt(2)
	s_nop 0
	v_mfma_f32_16x16x32_bf16 v[158:161], v[212:215], v[232:235], v[158:161]
	v_mfma_f32_16x16x32_bf16 v[154:157], v[216:219], v[232:235], v[154:157]
	v_mfma_f32_16x16x32_bf16 v[150:153], v[220:223], v[232:235], v[150:153]
	v_mfma_f32_16x16x32_bf16 v[146:149], v[224:227], v[232:235], v[146:149]
	ds_read_b128 v[232:235], v211 offset:0x2400
	s_waitcnt lgkmcnt(2)
	s_nop 0
	v_mfma_f32_16x16x32_bf16 v[142:145], v[212:215], v[236:239], v[142:145]
	v_mfma_f32_16x16x32_bf16 v[138:141], v[216:219], v[236:239], v[138:141]
	v_mfma_f32_16x16x32_bf16 v[134:137], v[220:223], v[236:239], v[134:137]
	v_mfma_f32_16x16x32_bf16 v[130:133], v[224:227], v[236:239], v[130:133]
	ds_read_b128 v[236:239], v211 offset:0x2c00
	s_waitcnt lgkmcnt(2)
	s_nop 0
	v_mfma_f32_16x16x32_bf16 v[126:129], v[212:215], v[228:231], v[126:129]
	v_mfma_f32_16x16x32_bf16 v[122:125], v[216:219], v[228:231], v[122:125]
	v_mfma_f32_16x16x32_bf16 v[118:121], v[220:223], v[228:231], v[118:121]
	v_mfma_f32_16x16x32_bf16 v[114:117], v[224:227], v[228:231], v[114:117]
	ds_read_b128 v[228:231], v211 offset:0x3400
	s_waitcnt lgkmcnt(2)
	s_nop 0
	v_mfma_f32_16x16x32_bf16 v[110:113], v[212:215], v[232:235], v[110:113]
	v_mfma_f32_16x16x32_bf16 v[106:109], v[216:219], v[232:235], v[106:109]
	v_mfma_f32_16x16x32_bf16 v[102:105], v[220:223], v[232:235], v[102:105]
	v_mfma_f32_16x16x32_bf16 v[98:101], v[224:227], v[232:235], v[98:101]
	ds_read_b128 v[232:235], v211 offset:0x3c00
	s_waitcnt lgkmcnt(2)
	s_nop 0
	v_mfma_f32_16x16x32_bf16 v[94:97], v[212:215], v[236:239], v[94:97]
	v_mfma_f32_16x16x32_bf16 v[90:93], v[216:219], v[236:239], v[90:93]
	v_mfma_f32_16x16x32_bf16 v[86:89], v[220:223], v[236:239], v[86:89]
	v_mfma_f32_16x16x32_bf16 v[82:85], v[224:227], v[236:239], v[82:85]
	s_waitcnt lgkmcnt(1)
	s_nop 0
	v_mfma_f32_16x16x32_bf16 v[78:81], v[212:215], v[228:231], v[78:81]
	v_mfma_f32_16x16x32_bf16 v[74:77], v[216:219], v[228:231], v[74:77]
	v_mfma_f32_16x16x32_bf16 v[70:73], v[220:223], v[228:231], v[70:73]
	v_mfma_f32_16x16x32_bf16 v[66:69], v[224:227], v[228:231], v[66:69]
	s_waitcnt lgkmcnt(0)
	s_nop 0
	v_mfma_f32_16x16x32_bf16 v[62:65], v[212:215], v[232:235], v[62:65]
	v_mfma_f32_16x16x32_bf16 v[58:61], v[216:219], v[232:235], v[58:61]
	v_mfma_f32_16x16x32_bf16 v[54:57], v[220:223], v[232:235], v[54:57]
	v_mfma_f32_16x16x32_bf16 v[50:53], v[224:227], v[232:235], v[50:53]
	s_waitcnt vmcnt(10)
	v_cvt_pk_bf16_f32 v22, v22, v23
	v_cvt_pk_bf16_f32 v23, v24, v25
	v_cvt_pk_bf16_f32 v24, v6, v7
	v_cvt_pk_bf16_f32 v25, v8, v9
	v_add_u32_e32 v6, s23, v204
	s_waitcnt vmcnt(9)
	v_cvt_pk_bf16_f32 v8, v2, v3
	v_add_u32_e32 v2, s23, v201
	ds_write_b128 v6, v[22:25]
	s_waitcnt vmcnt(8)
	v_cvt_pk_bf16_f32 v6, v10, v11
	v_cvt_pk_bf16_f32 v7, v12, v13
	v_cvt_pk_bf16_f32 v9, v4, v5
	ds_write_b128 v2, v[6:9]
	v_add_u32_e32 v2, s23, v202
	s_waitcnt vmcnt(7)
	ds_write_b128 v2, v[18:21] offset:32768
	v_add_u32_e32 v2, s23, v203
	s_waitcnt vmcnt(6)
	ds_write_b128 v2, v[14:17] offset:32768
	v_lshl_add_u64 v[2:3], s[20:21], 0, v[190:191]
	v_lshl_add_u64 v[2:3], v[2:3], 0, v[182:183]
	global_load_dwordx4 v[6:9], v[2:3], off offset:16
	global_load_dwordx4 v[22:25], v[2:3], off
	v_lshl_add_u64 v[2:3], s[20:21], 0, v[192:193]
	v_lshl_add_u64 v[14:15], s[0:1], 0, v[194:195]
	v_lshl_add_u64 v[16:17], s[0:1], 0, v[196:197]
	v_lshl_add_u64 v[10:11], v[2:3], 0, v[182:183]
	v_lshl_add_u64 v[14:15], v[14:15], 0, v[240:241]
	v_lshl_add_u64 v[16:17], v[16:17], 0, v[240:241]
	global_load_dwordx4 v[2:5], v[10:11], off offset:16
	s_nop 0
	global_load_dwordx4 v[10:13], v[10:11], off
	s_nop 0
	global_load_dwordx4 v[18:21], v[14:15], off
	s_nop 0
	global_load_dwordx4 v[14:17], v[16:17], off
	s_waitcnt lgkmcnt(0)
	s_add_i32 s22, s22, 64
	s_add_i32 s29, s29, 0x10000
	s_cmp_lg_u32 s29, 0xe0000
	s_barrier
	s_cbranch_scc1 .LBB1_1
	s_lshl_b64 s[0:1], s[18:19], 24
	ds_read_b128 v[180:183], v210 offset:0
	ds_read_b128 v[184:187], v210 offset:0x800
	ds_read_b128 v[188:191], v210 offset:0x1000
	ds_read_b128 v[192:195], v210 offset:0x1800
	ds_read_b128 v[212:215], v209 offset:0
	ds_read_b128 v[216:219], v209 offset:0x800
	ds_read_b128 v[220:223], v209 offset:0x1000
	s_waitcnt lgkmcnt(0)
	s_add_u32 s0, s10, s0
	s_addc_u32 s18, s11, s1
	s_lshl_b32 s19, s24, 1
	s_mov_b32 s1, 0
	s_add_u32 s0, s0, s19
	s_waitcnt lgkmcnt(2)
	s_addc_u32 s20, s18, 0
	v_mfma_f32_16x16x32_bf16 v[174:177], v[180:183], v[212:215], v[174:177]
	v_mfma_f32_16x16x32_bf16 v[170:173], v[184:187], v[212:215], v[170:173]
	v_mfma_f32_16x16x32_bf16 v[166:169], v[188:191], v[212:215], v[166:169]
	v_mfma_f32_16x16x32_bf16 v[162:165], v[192:195], v[212:215], v[162:165]
	ds_read_b128 v[212:215], v209 offset:0x1800
	s_waitcnt lgkmcnt(2)
	s_nop 0
	v_mfma_f32_16x16x32_bf16 v[158:161], v[180:183], v[216:219], v[158:161]
	v_mfma_f32_16x16x32_bf16 v[154:157], v[184:187], v[216:219], v[154:157]
	v_mfma_f32_16x16x32_bf16 v[150:153], v[188:191], v[216:219], v[150:153]
	v_mfma_f32_16x16x32_bf16 v[146:149], v[192:195], v[216:219], v[146:149]
	ds_read_b128 v[216:219], v209 offset:0x2000
	s_waitcnt lgkmcnt(2)
	s_nop 0
	v_mfma_f32_16x16x32_bf16 v[142:145], v[180:183], v[220:223], v[142:145]
	v_mfma_f32_16x16x32_bf16 v[138:141], v[184:187], v[220:223], v[138:141]
	v_mfma_f32_16x16x32_bf16 v[134:137], v[188:191], v[220:223], v[134:137]
	v_mfma_f32_16x16x32_bf16 v[130:133], v[192:195], v[220:223], v[130:133]
	ds_read_b128 v[220:223], v209 offset:0x2800
	s_waitcnt lgkmcnt(2)
	s_nop 0
	v_mfma_f32_16x16x32_bf16 v[126:129], v[180:183], v[212:215], v[126:129]
	v_mfma_f32_16x16x32_bf16 v[122:125], v[184:187], v[212:215], v[122:125]
	v_mfma_f32_16x16x32_bf16 v[118:121], v[188:191], v[212:215], v[118:121]
	v_mfma_f32_16x16x32_bf16 v[114:117], v[192:195], v[212:215], v[114:117]
	ds_read_b128 v[212:215], v209 offset:0x3000
	s_waitcnt lgkmcnt(2)
	s_nop 0
	v_mfma_f32_16x16x32_bf16 v[110:113], v[180:183], v[216:219], v[110:113]
	v_mfma_f32_16x16x32_bf16 v[106:109], v[184:187], v[216:219], v[106:109]
	v_mfma_f32_16x16x32_bf16 v[102:105], v[188:191], v[216:219], v[102:105]
	v_mfma_f32_16x16x32_bf16 v[98:101], v[192:195], v[216:219], v[98:101]
	ds_read_b128 v[216:219], v209 offset:0x3800
	s_waitcnt lgkmcnt(2)
	s_nop 0
	v_mfma_f32_16x16x32_bf16 v[94:97], v[180:183], v[220:223], v[94:97]
	v_mfma_f32_16x16x32_bf16 v[90:93], v[184:187], v[220:223], v[90:93]
	v_mfma_f32_16x16x32_bf16 v[86:89], v[188:191], v[220:223], v[86:89]
	v_mfma_f32_16x16x32_bf16 v[82:85], v[192:195], v[220:223], v[82:85]
	s_waitcnt lgkmcnt(1)
	s_nop 0
	v_mfma_f32_16x16x32_bf16 v[78:81], v[180:183], v[212:215], v[78:81]
	v_mfma_f32_16x16x32_bf16 v[74:77], v[184:187], v[212:215], v[74:77]
	v_mfma_f32_16x16x32_bf16 v[70:73], v[188:191], v[212:215], v[70:73]
	v_mfma_f32_16x16x32_bf16 v[66:69], v[192:195], v[212:215], v[66:69]
	s_waitcnt lgkmcnt(0)
	s_nop 0
	v_mfma_f32_16x16x32_bf16 v[62:65], v[180:183], v[216:219], v[62:65]
	v_mfma_f32_16x16x32_bf16 v[58:61], v[184:187], v[216:219], v[58:61]
	v_mfma_f32_16x16x32_bf16 v[54:57], v[188:191], v[216:219], v[54:57]
	v_mfma_f32_16x16x32_bf16 v[50:53], v[192:195], v[216:219], v[50:53]
	s_add_i32 s18, 0, 0x10000
	s_waitcnt vmcnt(10)
	v_cvt_pk_bf16_f32 v46, v46, v47
	v_cvt_pk_bf16_f32 v47, v48, v49
	v_cvt_pk_bf16_f32 v48, v42, v43
	v_add_u32_e32 v42, s18, v208
	s_waitcnt vmcnt(8)
	v_cvt_pk_bf16_f32 v38, v38, v39
	v_cvt_pk_bf16_f32 v39, v40, v41
	v_cvt_pk_bf16_f32 v40, v34, v35
	v_add_u32_e32 v34, s18, v205
	s_add_i32 s19, 0, 0x18000
	v_cvt_pk_bf16_f32 v49, v44, v45
	ds_write_b128 v42, v[46:49]
	v_cvt_pk_bf16_f32 v41, v36, v37
	ds_write_b128 v34, v[38:41]
	v_add_u32_e32 v34, s19, v206
	s_waitcnt vmcnt(7)
	ds_write_b128 v34, v[30:33]
	v_add_u32_e32 v30, s19, v207
	s_waitcnt vmcnt(6)
	ds_write_b128 v30, v[26:29]
	ds_read_b128 v[26:29], v210 offset:0x400
	ds_read_b128 v[30:33], v210 offset:0xc00
	ds_read_b128 v[34:37], v210 offset:0x1400
	ds_read_b128 v[38:41], v210 offset:0x1c00
	ds_read_b128 v[42:45], v209 offset:0x400
	ds_read_b128 v[46:49], v209 offset:0xc00
	ds_read_b128 v[180:183], v209 offset:0x1400
	s_nop 0
	s_waitcnt lgkmcnt(2)
	s_nop 0
	v_mfma_f32_16x16x32_bf16 v[174:177], v[26:29], v[42:45], v[174:177]
	v_mfma_f32_16x16x32_bf16 v[170:173], v[30:33], v[42:45], v[170:173]
	v_mfma_f32_16x16x32_bf16 v[166:169], v[34:37], v[42:45], v[166:169]
	v_mfma_f32_16x16x32_bf16 v[42:45], v[38:41], v[42:45], v[162:165]
	ds_read_b128 v[162:165], v209 offset:0x1c00
	s_waitcnt lgkmcnt(2)
	s_nop 0
	v_mfma_f32_16x16x32_bf16 v[158:161], v[26:29], v[46:49], v[158:161]
	v_mfma_f32_16x16x32_bf16 v[154:157], v[30:33], v[46:49], v[154:157]
	v_mfma_f32_16x16x32_bf16 v[150:153], v[34:37], v[46:49], v[150:153]
	v_mfma_f32_16x16x32_bf16 v[46:49], v[38:41], v[46:49], v[146:149]
	ds_read_b128 v[146:149], v209 offset:0x2400
	s_waitcnt lgkmcnt(2)
	s_nop 0
	v_mfma_f32_16x16x32_bf16 v[142:145], v[26:29], v[180:183], v[142:145]
	v_mfma_f32_16x16x32_bf16 v[138:141], v[30:33], v[180:183], v[138:141]
	v_mfma_f32_16x16x32_bf16 v[134:137], v[34:37], v[180:183], v[134:137]
	v_mfma_f32_16x16x32_bf16 v[130:133], v[38:41], v[180:183], v[130:133]
	ds_read_b128 v[180:183], v209 offset:0x2c00
	s_waitcnt lgkmcnt(2)
	s_nop 0
	v_mfma_f32_16x16x32_bf16 v[126:129], v[26:29], v[162:165], v[126:129]
	v_mfma_f32_16x16x32_bf16 v[122:125], v[30:33], v[162:165], v[122:125]
	v_mfma_f32_16x16x32_bf16 v[118:121], v[34:37], v[162:165], v[118:121]
	v_mfma_f32_16x16x32_bf16 v[114:117], v[38:41], v[162:165], v[114:117]
	ds_read_b128 v[162:165], v209 offset:0x3400
	s_waitcnt lgkmcnt(2)
	s_nop 0
	v_mfma_f32_16x16x32_bf16 v[110:113], v[26:29], v[146:149], v[110:113]
	v_mfma_f32_16x16x32_bf16 v[106:109], v[30:33], v[146:149], v[106:109]
	v_mfma_f32_16x16x32_bf16 v[102:105], v[34:37], v[146:149], v[102:105]
	v_mfma_f32_16x16x32_bf16 v[98:101], v[38:41], v[146:149], v[98:101]
	ds_read_b128 v[146:149], v209 offset:0x3c00
	s_waitcnt lgkmcnt(2)
	s_nop 0
	v_mfma_f32_16x16x32_bf16 v[94:97], v[26:29], v[180:183], v[94:97]
	v_mfma_f32_16x16x32_bf16 v[90:93], v[30:33], v[180:183], v[90:93]
	v_mfma_f32_16x16x32_bf16 v[86:89], v[34:37], v[180:183], v[86:89]
	v_mfma_f32_16x16x32_bf16 v[82:85], v[38:41], v[180:183], v[82:85]
	s_waitcnt lgkmcnt(1)
	s_nop 0
	v_mfma_f32_16x16x32_bf16 v[78:81], v[26:29], v[162:165], v[78:81]
	v_mfma_f32_16x16x32_bf16 v[74:77], v[30:33], v[162:165], v[74:77]
	v_mfma_f32_16x16x32_bf16 v[70:73], v[34:37], v[162:165], v[70:73]
	v_mfma_f32_16x16x32_bf16 v[66:69], v[38:41], v[162:165], v[66:69]
	s_waitcnt lgkmcnt(0)
	s_nop 0
	v_mfma_f32_16x16x32_bf16 v[26:29], v[26:29], v[146:149], v[62:65]
	v_mfma_f32_16x16x32_bf16 v[30:33], v[30:33], v[146:149], v[58:61]
	v_mfma_f32_16x16x32_bf16 v[34:37], v[34:37], v[146:149], v[54:57]
	v_mfma_f32_16x16x32_bf16 v[38:41], v[38:41], v[146:149], v[50:53]
	s_waitcnt vmcnt(4)
	v_cvt_pk_bf16_f32 v22, v22, v23
	v_cvt_pk_bf16_f32 v23, v24, v25
	v_cvt_pk_bf16_f32 v24, v6, v7
	v_cvt_pk_bf16_f32 v25, v8, v9
	v_add_u32_e32 v6, s18, v204
	s_waitcnt vmcnt(3)
	v_cvt_pk_bf16_f32 v8, v2, v3
	v_add_u32_e32 v2, s18, v201
	ds_write_b128 v6, v[22:25]
	s_waitcnt vmcnt(2)
	v_cvt_pk_bf16_f32 v6, v10, v11
	v_cvt_pk_bf16_f32 v7, v12, v13
	v_cvt_pk_bf16_f32 v9, v4, v5
	ds_write_b128 v2, v[6:9]
	v_add_u32_e32 v2, s19, v202
	s_waitcnt vmcnt(1)
	ds_write_b128 v2, v[18:21]
	v_add_u32_e32 v2, s19, v203
	s_waitcnt vmcnt(0)
	ds_write_b128 v2, v[14:17]
	s_waitcnt lgkmcnt(0)
	s_barrier
	v_add_u32_e32 v178, 0x10000, v209
	v_add_u32_e32 v196, 0x10000, v210
	ds_read_b128 v[2:5], v196 offset:0
	ds_read_b128 v[6:9], v196 offset:0x800
	ds_read_b128 v[10:13], v196 offset:0x1000
	ds_read_b128 v[14:17], v196 offset:0x1800
	ds_read_b128 v[18:21], v178 offset:0
	s_and_b64 s[16:17], s[16:17], exec
	ds_read_b128 v[22:25], v178 offset:0x800
	ds_read_b128 v[50:53], v178 offset:0x1000
	s_waitcnt lgkmcnt(2)
	s_cselect_b32 s5, s5, s7
	s_cselect_b32 s4, s4, s6
	s_lshl_b32 s6, s3, 10
	v_mfma_f32_16x16x32_bf16 v[54:57], v[2:5], v[18:21], v[174:177]
	s_add_u32 s6, s4, s6
	s_addc_u32 s7, s5, 0
	s_lshl_b32 s3, s3, 9
	v_mfma_f32_16x16x32_bf16 v[58:61], v[6:9], v[18:21], v[170:173]
	s_add_u32 s4, s0, s3
	s_addc_u32 s5, s20, 0
	v_mfma_f32_16x16x32_bf16 v[62:65], v[10:13], v[18:21], v[166:169]
	v_mfma_f32_16x16x32_bf16 v[18:21], v[14:17], v[18:21], v[42:45]
	ds_read_b128 v[42:45], v178 offset:0x1800
	s_waitcnt lgkmcnt(2)
	s_nop 0
	v_mfma_f32_16x16x32_bf16 v[146:149], v[2:5], v[22:25], v[158:161]
	v_mfma_f32_16x16x32_bf16 v[154:157], v[6:9], v[22:25], v[154:157]
	v_mfma_f32_16x16x32_bf16 v[150:153], v[10:13], v[22:25], v[150:153]
	v_mfma_f32_16x16x32_bf16 v[22:25], v[14:17], v[22:25], v[46:49]
	ds_read_b128 v[46:49], v178 offset:0x2000
	s_waitcnt lgkmcnt(2)
	s_nop 0
	v_mfma_f32_16x16x32_bf16 v[142:145], v[2:5], v[50:53], v[142:145]
	v_mfma_f32_16x16x32_bf16 v[138:141], v[6:9], v[50:53], v[138:141]
	v_mfma_f32_16x16x32_bf16 v[134:137], v[10:13], v[50:53], v[134:137]
	v_mfma_f32_16x16x32_bf16 v[50:53], v[14:17], v[50:53], v[130:133]
	ds_read_b128 v[130:133], v178 offset:0x2800
	s_waitcnt lgkmcnt(2)
	s_nop 0
	v_mfma_f32_16x16x32_bf16 v[126:129], v[2:5], v[42:45], v[126:129]
	v_mfma_f32_16x16x32_bf16 v[122:125], v[6:9], v[42:45], v[122:125]
	v_mfma_f32_16x16x32_bf16 v[118:121], v[10:13], v[42:45], v[118:121]
	v_mfma_f32_16x16x32_bf16 v[42:45], v[14:17], v[42:45], v[114:117]
	ds_read_b128 v[114:117], v178 offset:0x3000
	s_waitcnt lgkmcnt(2)
	s_nop 0
	v_mfma_f32_16x16x32_bf16 v[110:113], v[2:5], v[46:49], v[110:113]
	v_mfma_f32_16x16x32_bf16 v[106:109], v[6:9], v[46:49], v[106:109]
	v_mfma_f32_16x16x32_bf16 v[102:105], v[10:13], v[46:49], v[102:105]
	v_mfma_f32_16x16x32_bf16 v[98:101], v[14:17], v[46:49], v[98:101]
	ds_read_b128 v[46:49], v178 offset:0x3800
	s_waitcnt lgkmcnt(2)
	s_nop 0
	v_mfma_f32_16x16x32_bf16 v[158:161], v[2:5], v[130:133], v[94:97]
	v_mfma_f32_16x16x32_bf16 v[162:165], v[6:9], v[130:133], v[90:93]
	v_mfma_f32_16x16x32_bf16 v[166:169], v[10:13], v[130:133], v[86:89]
	v_mfma_f32_16x16x32_bf16 v[130:133], v[14:17], v[130:133], v[82:85]
	s_waitcnt lgkmcnt(1)
	s_nop 0
	v_mfma_f32_16x16x32_bf16 v[66:69], v[14:17], v[114:117], v[66:69]
	v_mfma_f32_16x16x32_bf16 v[170:173], v[2:5], v[114:117], v[78:81]
	v_mfma_f32_16x16x32_bf16 v[174:177], v[6:9], v[114:117], v[74:77]
	v_mfma_f32_16x16x32_bf16 v[180:183], v[10:13], v[114:117], v[70:73]
	s_waitcnt lgkmcnt(0)
	s_nop 0
	v_mfma_f32_16x16x32_bf16 v[2:5], v[2:5], v[46:49], v[26:29]
	v_mfma_f32_16x16x32_bf16 v[114:117], v[6:9], v[46:49], v[30:33]
	v_mfma_f32_16x16x32_bf16 v[34:37], v[10:13], v[46:49], v[34:37]
	v_mfma_f32_16x16x32_bf16 v[184:187], v[14:17], v[46:49], v[38:41]
	ds_read_b128 v[188:191], v196 offset:0x400
	ds_read_b128 v[192:195], v196 offset:0xc00
	ds_read_b128 v[202:205], v196 offset:0x1400
	ds_read_b128 v[206:209], v196 offset:0x1c00
	ds_read_b128 v[6:9], v178 offset:0x400
	ds_read_b128 v[10:13], v178 offset:0xc00
	ds_read_b128 v[14:17], v178 offset:0x1400
	s_nop 0
	s_waitcnt lgkmcnt(2)
	s_nop 0
	v_mfma_f32_16x16x32_bf16 v[94:97], v[192:195], v[6:9], v[58:61]
	v_mfma_f32_16x16x32_bf16 v[62:65], v[202:205], v[6:9], v[62:65]
	v_mfma_f32_16x16x32_bf16 v[30:33], v[206:209], v[6:9], v[18:21]
	v_mfma_f32_16x16x32_bf16 v[210:213], v[188:191], v[6:9], v[54:57]
	ds_read_b128 v[6:9], v178 offset:0x1c00
	s_waitcnt lgkmcnt(2)
	s_nop 0
	v_mfma_f32_16x16x32_bf16 v[90:93], v[192:195], v[10:13], v[154:157]
	v_mfma_f32_16x16x32_bf16 v[58:61], v[202:205], v[10:13], v[150:153]
	v_mfma_f32_16x16x32_bf16 v[26:29], v[206:209], v[10:13], v[22:25]
	v_mfma_f32_16x16x32_bf16 v[146:149], v[188:191], v[10:13], v[146:149]
	ds_read_b128 v[10:13], v178 offset:0x2400
	s_waitcnt lgkmcnt(2)
	s_nop 0
	v_mfma_f32_16x16x32_bf16 v[86:89], v[192:195], v[14:17], v[138:141]
	v_mfma_f32_16x16x32_bf16 v[54:57], v[202:205], v[14:17], v[134:137]
	v_mfma_f32_16x16x32_bf16 v[22:25], v[206:209], v[14:17], v[50:53]
	v_mfma_f32_16x16x32_bf16 v[142:145], v[188:191], v[14:17], v[142:145]
	ds_read_b128 v[38:41], v178 offset:0x2c00
	s_waitcnt lgkmcnt(2)
	s_nop 0
	v_mfma_f32_16x16x32_bf16 v[126:129], v[188:191], v[6:9], v[126:129]
	v_mfma_f32_16x16x32_bf16 v[82:85], v[192:195], v[6:9], v[122:125]
	v_mfma_f32_16x16x32_bf16 v[50:53], v[202:205], v[6:9], v[118:121]
	v_mfma_f32_16x16x32_bf16 v[18:21], v[206:209], v[6:9], v[42:45]
	ds_read_b128 v[6:9], v178 offset:0x3400
	s_waitcnt lgkmcnt(2)
	s_nop 0
	v_mfma_f32_16x16x32_bf16 v[110:113], v[188:191], v[10:13], v[110:113]
	v_mfma_f32_16x16x32_bf16 v[78:81], v[192:195], v[10:13], v[106:109]
	v_mfma_f32_16x16x32_bf16 v[46:49], v[202:205], v[10:13], v[102:105]
	v_mfma_f32_16x16x32_bf16 v[14:17], v[206:209], v[10:13], v[98:101]
	ds_read_b128 v[98:101], v178 offset:0x3c00
	s_waitcnt lgkmcnt(2)
	s_nop 0
	v_mfma_f32_16x16x32_bf16 v[106:109], v[188:191], v[38:41], v[158:161]
	v_mfma_f32_16x16x32_bf16 v[74:77], v[192:195], v[38:41], v[162:165]
	v_mfma_f32_16x16x32_bf16 v[42:45], v[202:205], v[38:41], v[166:169]
	v_mfma_f32_16x16x32_bf16 v[10:13], v[206:209], v[38:41], v[130:133]
	s_waitcnt lgkmcnt(1)
	s_nop 0
	v_mfma_f32_16x16x32_bf16 v[118:121], v[188:191], v[6:9], v[170:173]
	v_mfma_f32_16x16x32_bf16 v[70:73], v[192:195], v[6:9], v[174:177]
	v_mfma_f32_16x16x32_bf16 v[38:41], v[202:205], v[6:9], v[180:183]
	v_mfma_f32_16x16x32_bf16 v[6:9], v[206:209], v[6:9], v[66:69]
	s_waitcnt lgkmcnt(0)
	s_nop 0
	v_mfma_f32_16x16x32_bf16 v[122:125], v[188:191], v[98:101], v[2:5]
	v_mfma_f32_16x16x32_bf16 v[66:69], v[192:195], v[98:101], v[114:117]
	v_mfma_f32_16x16x32_bf16 v[34:37], v[202:205], v[98:101], v[34:37]
	v_mfma_f32_16x16x32_bf16 v[2:5], v[206:209], v[98:101], v[184:187]
	v_lshrrev_b32_e32 v98, 2, v199
	v_and_b32_e32 v98, 12, v98
	v_lshl_or_b32 v104, v200, 6, v98
	v_lshlrev_b32_e32 v105, 2, v104
	s_waitcnt lgkmcnt(0)
	s_barrier
	global_load_dwordx4 v[114:117], v105, s[6:7]
	v_lshrrev_b32_e32 v98, 1, v199
	v_lshlrev_b32_e32 v99, 16, v198
	v_lshlrev_b32_e32 v100, 9, v179
	v_and_b32_e32 v102, 8, v98
	v_lshrrev_b32_e32 v98, 3, v104
	v_add3_u32 v103, 0, v99, v100
	v_xor_b32_e32 v130, v98, v179
	v_bitop3_b32 v131, v98, v179, 16 bitop3:0x1e
	global_load_dwordx4 v[98:101], v105, s[6:7] offset:64
	v_lshlrev_b32_e32 v130, 4, v130
	v_lshlrev_b32_e32 v131, 4, v131
	v_add3_u32 v130, v103, v130, v102
	v_add3_u32 v131, v103, v131, v102
	s_movk_i32 s0, 0x200
	s_waitcnt vmcnt(1)
	v_add_f32_e32 v132, v210, v114
	v_add_f32_e32 v133, v211, v115
	v_add_f32_e32 v134, v212, v116
	v_add_f32_e32 v135, v213, v117
	v_add_f32_e32 v140, v142, v114
	v_add_f32_e32 v141, v143, v115
	v_add_f32_e32 v142, v144, v116
	v_add_f32_e32 v143, v145, v117
	v_add_f32_e32 v110, v110, v114
	v_add_f32_e32 v111, v111, v115
	v_add_f32_e32 v106, v106, v114
	v_add_f32_e32 v107, v107, v115
	v_add_f32_e32 v136, v146, v114
	v_add_f32_e32 v137, v147, v115
	v_add_f32_e32 v138, v148, v116
	v_add_f32_e32 v139, v149, v117
	v_add_f32_e32 v126, v126, v114
	v_add_f32_e32 v127, v127, v115
	v_add_f32_e32 v128, v128, v116
	v_add_f32_e32 v129, v129, v117
	v_add_f32_e32 v112, v112, v116
	v_add_f32_e32 v113, v113, v117
	v_add_f32_e32 v108, v108, v116
	v_add_f32_e32 v109, v109, v117
	v_max_f32_e32 v132, 0, v132
	v_max_f32_e32 v133, 0, v133
	v_max_f32_e32 v134, 0, v134
	v_max_f32_e32 v135, 0, v135
	v_max_f32_e32 v140, 0, v140
	v_max_f32_e32 v141, 0, v141
	v_max_f32_e32 v142, 0, v142
	v_max_f32_e32 v143, 0, v143
	v_max_f32_e32 v144, 0, v110
	v_max_f32_e32 v145, 0, v111
	v_max_f32_e32 v148, 0, v106
	v_max_f32_e32 v149, 0, v107
	v_cvt_pk_bf16_f32 v106, v132, v133
	v_cvt_pk_bf16_f32 v107, v134, v135
	v_cvt_pk_bf16_f32 v110, v140, v141
	v_cvt_pk_bf16_f32 v111, v142, v143
	v_add_f32_e32 v118, v118, v114
	v_add_f32_e32 v119, v119, v115
	v_max_f32_e32 v136, 0, v136
	v_max_f32_e32 v137, 0, v137
	v_max_f32_e32 v138, 0, v138
	v_max_f32_e32 v139, 0, v139
	v_max_f32_e32 v126, 0, v126
	v_max_f32_e32 v127, 0, v127
	v_max_f32_e32 v128, 0, v128
	v_max_f32_e32 v129, 0, v129
	v_max_f32_e32 v146, 0, v112
	v_max_f32_e32 v147, 0, v113
	v_max_f32_e32 v150, 0, v108
	v_max_f32_e32 v151, 0, v109
	v_cvt_pk_bf16_f32 v108, v136, v137
	v_cvt_pk_bf16_f32 v109, v138, v139
	v_cvt_pk_bf16_f32 v112, v126, v127
	v_cvt_pk_bf16_f32 v113, v128, v129
	ds_write2st64_b64 v130, v[106:107], v[110:111] offset1:32
	ds_write2st64_b64 v131, v[108:109], v[112:113] offset0:16 offset1:48
	v_add_f32_e32 v106, v121, v117
	v_add_f32_e32 v120, v120, v116
	v_max_f32_e32 v152, 0, v118
	v_max_f32_e32 v153, 0, v119
	v_max_f32_e32 v107, 0, v106
	v_cvt_pk_bf16_f32 v106, v152, v153
	v_max_f32_e32 v120, 0, v120
	v_cvt_pk_bf16_f32 v118, v144, v145
	v_cvt_pk_bf16_f32 v119, v146, v147
	v_cvt_pk_bf16_f32 v107, v120, v107
	ds_write2st64_b64 v130, v[118:119], v[106:107] offset0:64 offset1:96
	v_add_f32_e32 v106, v122, v114
	v_max_f32_e32 v106, 0, v106
	v_add_f32_e32 v107, v123, v115
	v_max_f32_e32 v107, 0, v107
	v_add_f32_e32 v108, v124, v116
	v_add_f32_e32 v109, v125, v117
	v_cvt_pk_bf16_f32 v106, v106, v107
	v_cvt_pk_bf16_f32 v126, v148, v149
	v_cvt_pk_bf16_f32 v127, v150, v151
	v_max_f32_e32 v108, 0, v108
	v_max_f32_e32 v109, 0, v109
	v_cvt_pk_bf16_f32 v107, v108, v109
	ds_write2st64_b64 v131, v[126:127], v[106:107] offset0:80 offset1:112
	v_or_b32_e32 v106, 16, v104
	s_waitcnt vmcnt(0)
	v_add_f32_e32 v94, v94, v98
	v_add_f32_e32 v95, v95, v99
	v_add_f32_e32 v96, v96, v100
	v_lshrrev_b32_e32 v106, 3, v106
	v_max_f32_e32 v94, 0, v94
	v_max_f32_e32 v95, 0, v95
	v_max_f32_e32 v96, 0, v96
	v_add_f32_e32 v97, v97, v101
	v_max_f32_e32 v97, 0, v97
	v_cvt_pk_bf16_f32 v94, v94, v95
	v_cvt_pk_bf16_f32 v95, v96, v97
	v_xor_b32_e32 v96, v106, v179
	v_lshlrev_b32_e32 v96, 4, v96
	v_add3_u32 v107, v103, v96, v102
	v_add_f32_e32 v90, v90, v98
	v_add_f32_e32 v91, v91, v99
	v_add_f32_e32 v92, v92, v100
	ds_write_b64 v107, v[94:95]
	v_max_f32_e32 v90, 0, v90
	v_max_f32_e32 v91, 0, v91
	global_load_dwordx4 v[94:97], v105, s[6:7] offset:128
	v_max_f32_e32 v92, 0, v92
	v_add_f32_e32 v93, v93, v101
	v_max_f32_e32 v93, 0, v93
	v_cvt_pk_bf16_f32 v90, v90, v91
	v_cvt_pk_bf16_f32 v91, v92, v93
	v_bitop3_b32 v92, v106, v179, 16 bitop3:0x1e
	v_add_f32_e32 v66, v66, v98
	v_lshlrev_b32_e32 v92, 4, v92
	v_add_f32_e32 v86, v86, v98
	v_add_f32_e32 v87, v87, v99
	v_add_f32_e32 v82, v82, v98
	v_add_f32_e32 v83, v83, v99
	v_add_f32_e32 v78, v78, v98
	v_add_f32_e32 v79, v79, v99
	v_add_f32_e32 v74, v74, v98
	v_add_f32_e32 v75, v75, v99
	v_add_f32_e32 v70, v70, v98
	v_add_f32_e32 v71, v71, v99
	v_max_f32_e32 v66, 0, v66
	v_add_f32_e32 v67, v67, v99
	v_add3_u32 v92, v103, v92, v102
	v_max_f32_e32 v86, 0, v86
	v_max_f32_e32 v87, 0, v87
	v_add_f32_e32 v88, v88, v100
	v_add_f32_e32 v89, v89, v101
	v_max_f32_e32 v82, 0, v82
	v_max_f32_e32 v83, 0, v83
	v_add_f32_e32 v84, v84, v100
	v_add_f32_e32 v85, v85, v101
	v_max_f32_e32 v78, 0, v78
	v_max_f32_e32 v79, 0, v79
	v_add_f32_e32 v80, v80, v100
	v_add_f32_e32 v81, v81, v101
	v_max_f32_e32 v74, 0, v74
	v_max_f32_e32 v75, 0, v75
	v_add_f32_e32 v76, v76, v100
	v_add_f32_e32 v77, v77, v101
	v_max_f32_e32 v70, 0, v70
	v_max_f32_e32 v71, 0, v71
	v_add_f32_e32 v72, v72, v100
	v_add_f32_e32 v73, v73, v101
	v_max_f32_e32 v67, 0, v67
	v_add_f32_e32 v68, v68, v100
	v_add_f32_e32 v69, v69, v101
	v_cvt_pk_bf16_f32 v66, v66, v67
	ds_write_b64 v92, v[90:91] offset:8192
	v_max_f32_e32 v88, 0, v88
	v_max_f32_e32 v89, 0, v89
	v_cvt_pk_bf16_f32 v86, v86, v87
	v_cvt_pk_bf16_f32 v87, v88, v89
	ds_write_b64 v107, v[86:87] offset:16384
	v_max_f32_e32 v84, 0, v84
	v_max_f32_e32 v85, 0, v85
	v_cvt_pk_bf16_f32 v82, v82, v83
	v_cvt_pk_bf16_f32 v83, v84, v85
	ds_write_b64 v92, v[82:83] offset:24576
	v_max_f32_e32 v80, 0, v80
	v_max_f32_e32 v81, 0, v81
	v_cvt_pk_bf16_f32 v78, v78, v79
	v_cvt_pk_bf16_f32 v79, v80, v81
	ds_write_b64 v107, v[78:79] offset:32768
	v_max_f32_e32 v76, 0, v76
	v_max_f32_e32 v77, 0, v77
	v_cvt_pk_bf16_f32 v74, v74, v75
	v_cvt_pk_bf16_f32 v75, v76, v77
	ds_write_b64 v92, v[74:75] offset:40960
	v_max_f32_e32 v72, 0, v72
	v_max_f32_e32 v73, 0, v73
	v_cvt_pk_bf16_f32 v70, v70, v71
	v_cvt_pk_bf16_f32 v71, v72, v73
	ds_write_b64 v107, v[70:71] offset:49152
	v_max_f32_e32 v68, 0, v68
	v_max_f32_e32 v69, 0, v69
	v_cvt_pk_bf16_f32 v67, v68, v69
	ds_write_b64 v92, v[66:67] offset:57344
	v_or_b32_e32 v66, 32, v104
	v_lshrrev_b32_e32 v70, 3, v66
	global_load_dwordx4 v[66:69], v105, s[6:7] offset:192
	s_waitcnt vmcnt(1)
	v_add_f32_e32 v62, v62, v94
	v_add_f32_e32 v63, v63, v95
	v_add_f32_e32 v64, v64, v96
	v_add_f32_e32 v58, v58, v94
	v_add_f32_e32 v59, v59, v95
	v_add_f32_e32 v60, v60, v96
	v_max_f32_e32 v62, 0, v62
	v_max_f32_e32 v63, 0, v63
	v_max_f32_e32 v64, 0, v64
	v_add_f32_e32 v65, v65, v97
	v_max_f32_e32 v58, 0, v58
	v_max_f32_e32 v59, 0, v59
	v_max_f32_e32 v60, 0, v60
	v_add_f32_e32 v61, v61, v97
	v_max_f32_e32 v65, 0, v65
	v_cvt_pk_bf16_f32 v62, v62, v63
	v_cvt_pk_bf16_f32 v63, v64, v65
	v_xor_b32_e32 v64, v70, v179
	v_max_f32_e32 v61, 0, v61
	v_cvt_pk_bf16_f32 v58, v58, v59
	v_cvt_pk_bf16_f32 v59, v60, v61
	v_bitop3_b32 v60, v70, v179, 16 bitop3:0x1e
	v_add_f32_e32 v34, v34, v94
	v_lshlrev_b32_e32 v64, 4, v64
	v_lshlrev_b32_e32 v60, 4, v60
	v_add_f32_e32 v54, v54, v94
	v_add_f32_e32 v55, v55, v95
	v_add_f32_e32 v50, v50, v94
	v_add_f32_e32 v51, v51, v95
	v_add_f32_e32 v46, v46, v94
	v_add_f32_e32 v47, v47, v95
	v_add_f32_e32 v42, v42, v94
	v_add_f32_e32 v43, v43, v95
	v_add_f32_e32 v38, v38, v94
	v_add_f32_e32 v39, v39, v95
	v_max_f32_e32 v34, 0, v34
	v_add_f32_e32 v35, v35, v95
	v_add3_u32 v64, v103, v64, v102
	v_add3_u32 v60, v103, v60, v102
	v_max_f32_e32 v54, 0, v54
	v_max_f32_e32 v55, 0, v55
	v_add_f32_e32 v56, v56, v96
	v_add_f32_e32 v57, v57, v97
	v_max_f32_e32 v50, 0, v50
	v_max_f32_e32 v51, 0, v51
	v_add_f32_e32 v52, v52, v96
	v_add_f32_e32 v53, v53, v97
	v_max_f32_e32 v46, 0, v46
	v_max_f32_e32 v47, 0, v47
	v_add_f32_e32 v48, v48, v96
	v_add_f32_e32 v49, v49, v97
	v_max_f32_e32 v42, 0, v42
	v_max_f32_e32 v43, 0, v43
	v_add_f32_e32 v44, v44, v96
	v_add_f32_e32 v45, v45, v97
	v_max_f32_e32 v38, 0, v38
	v_max_f32_e32 v39, 0, v39
	v_add_f32_e32 v40, v40, v96
	v_add_f32_e32 v41, v41, v97
	v_max_f32_e32 v35, 0, v35
	v_add_f32_e32 v36, v36, v96
	v_add_f32_e32 v37, v37, v97
	v_cvt_pk_bf16_f32 v34, v34, v35
	ds_write_b64 v64, v[62:63]
	ds_write_b64 v60, v[58:59] offset:8192
	v_max_f32_e32 v56, 0, v56
	v_max_f32_e32 v57, 0, v57
	v_cvt_pk_bf16_f32 v54, v54, v55
	v_cvt_pk_bf16_f32 v55, v56, v57
	ds_write_b64 v64, v[54:55] offset:16384
	v_max_f32_e32 v52, 0, v52
	v_max_f32_e32 v53, 0, v53
	v_cvt_pk_bf16_f32 v50, v50, v51
	v_cvt_pk_bf16_f32 v51, v52, v53
	ds_write_b64 v60, v[50:51] offset:24576
	v_max_f32_e32 v48, 0, v48
	v_max_f32_e32 v49, 0, v49
	v_cvt_pk_bf16_f32 v46, v46, v47
	v_cvt_pk_bf16_f32 v47, v48, v49
	ds_write_b64 v64, v[46:47] offset:32768
	v_max_f32_e32 v44, 0, v44
	v_max_f32_e32 v45, 0, v45
	v_cvt_pk_bf16_f32 v42, v42, v43
	v_cvt_pk_bf16_f32 v43, v44, v45
	ds_write_b64 v60, v[42:43] offset:40960
	v_max_f32_e32 v40, 0, v40
	v_max_f32_e32 v41, 0, v41
	v_cvt_pk_bf16_f32 v38, v38, v39
	v_cvt_pk_bf16_f32 v39, v40, v41
	ds_write_b64 v64, v[38:39] offset:49152
	v_max_f32_e32 v36, 0, v36
	v_max_f32_e32 v37, 0, v37
	v_cvt_pk_bf16_f32 v35, v36, v37
	ds_write_b64 v60, v[34:35] offset:57344
	v_or_b32_e32 v34, 48, v104
	s_waitcnt vmcnt(0)
	v_add_f32_e32 v30, v30, v66
	v_add_f32_e32 v31, v31, v67
	v_add_f32_e32 v32, v32, v68
	v_add_f32_e32 v26, v26, v66
	v_add_f32_e32 v27, v27, v67
	v_add_f32_e32 v28, v28, v68
	v_lshrrev_b32_e32 v34, 3, v34
	v_max_f32_e32 v30, 0, v30
	v_max_f32_e32 v31, 0, v31
	v_max_f32_e32 v32, 0, v32
	v_add_f32_e32 v33, v33, v69
	v_max_f32_e32 v26, 0, v26
	v_max_f32_e32 v27, 0, v27
	v_max_f32_e32 v28, 0, v28
	v_add_f32_e32 v29, v29, v69
	v_max_f32_e32 v33, 0, v33
	v_cvt_pk_bf16_f32 v30, v30, v31
	v_cvt_pk_bf16_f32 v31, v32, v33
	v_xor_b32_e32 v32, v34, v179
	v_max_f32_e32 v29, 0, v29
	v_cvt_pk_bf16_f32 v26, v26, v27
	v_cvt_pk_bf16_f32 v27, v28, v29
	v_bitop3_b32 v28, v34, v179, 16 bitop3:0x1e
	v_add_f32_e32 v2, v2, v66
	v_lshlrev_b32_e32 v32, 4, v32
	v_lshlrev_b32_e32 v28, 4, v28
	v_add_f32_e32 v22, v22, v66
	v_add_f32_e32 v23, v23, v67
	v_add_f32_e32 v18, v18, v66
	v_add_f32_e32 v19, v19, v67
	v_add_f32_e32 v14, v14, v66
	v_add_f32_e32 v15, v15, v67
	v_add_f32_e32 v10, v10, v66
	v_add_f32_e32 v11, v11, v67
	v_add_f32_e32 v6, v6, v66
	v_add_f32_e32 v7, v7, v67
	v_max_f32_e32 v2, 0, v2
	v_add_f32_e32 v3, v3, v67
	v_add3_u32 v32, v103, v32, v102
	v_add3_u32 v28, v103, v28, v102
	v_max_f32_e32 v22, 0, v22
	v_max_f32_e32 v23, 0, v23
	v_add_f32_e32 v24, v24, v68
	v_add_f32_e32 v25, v25, v69
	v_max_f32_e32 v18, 0, v18
	v_max_f32_e32 v19, 0, v19
	v_add_f32_e32 v20, v20, v68
	v_add_f32_e32 v21, v21, v69
	v_max_f32_e32 v14, 0, v14
	v_max_f32_e32 v15, 0, v15
	v_add_f32_e32 v16, v16, v68
	v_add_f32_e32 v17, v17, v69
	v_max_f32_e32 v10, 0, v10
	v_max_f32_e32 v11, 0, v11
	v_add_f32_e32 v12, v12, v68
	v_add_f32_e32 v13, v13, v69
	v_max_f32_e32 v6, 0, v6
	v_max_f32_e32 v7, 0, v7
	v_add_f32_e32 v8, v8, v68
	v_add_f32_e32 v9, v9, v69
	v_max_f32_e32 v3, 0, v3
	v_add_f32_e32 v4, v4, v68
	v_add_f32_e32 v5, v5, v69
	v_cvt_pk_bf16_f32 v2, v2, v3
	ds_write_b64 v32, v[30:31]
	ds_write_b64 v28, v[26:27] offset:8192
	v_max_f32_e32 v24, 0, v24
	v_max_f32_e32 v25, 0, v25
	v_cvt_pk_bf16_f32 v22, v22, v23
	v_cvt_pk_bf16_f32 v23, v24, v25
	ds_write_b64 v32, v[22:23] offset:16384
	v_max_f32_e32 v20, 0, v20
	v_max_f32_e32 v21, 0, v21
	v_cvt_pk_bf16_f32 v18, v18, v19
	v_cvt_pk_bf16_f32 v19, v20, v21
	ds_write_b64 v28, v[18:19] offset:24576
	v_max_f32_e32 v16, 0, v16
	v_max_f32_e32 v17, 0, v17
	v_cvt_pk_bf16_f32 v14, v14, v15
	v_cvt_pk_bf16_f32 v15, v16, v17
	ds_write_b64 v32, v[14:15] offset:32768
	v_max_f32_e32 v12, 0, v12
	v_max_f32_e32 v13, 0, v13
	v_cvt_pk_bf16_f32 v10, v10, v11
	v_cvt_pk_bf16_f32 v11, v12, v13
	ds_write_b64 v28, v[10:11] offset:40960
	v_max_f32_e32 v8, 0, v8
	v_max_f32_e32 v9, 0, v9
	v_cvt_pk_bf16_f32 v6, v6, v7
	v_cvt_pk_bf16_f32 v7, v8, v9
	ds_write_b64 v32, v[6:7] offset:49152
	v_max_f32_e32 v4, 0, v4
	v_max_f32_e32 v5, 0, v5
	v_cvt_pk_bf16_f32 v3, v4, v5
	ds_write_b64 v28, v[2:3] offset:57344
	v_and_b32_e32 v2, 0x1f0, v1
	v_lshrrev_b32_e32 v1, 5, v0
	v_xor_b32_e32 v4, v1, v0
	v_mov_b32_e32 v3, 0
	v_lshlrev_b32_e32 v4, 4, v4
	v_lshl_add_u64 v[12:13], s[4:5], 0, v[2:3]
	v_lshlrev_b32_e32 v2, 9, v1
	v_and_b32_e32 v16, 0x1f0, v4
	v_add3_u32 v2, 0, v2, v16
	s_waitcnt lgkmcnt(0)
	s_barrier
	ds_read_b128 v[4:7], v2
	v_lshlrev_b32_e32 v2, 11, v1
	v_lshl_add_u64 v[14:15], v[12:13], 0, v[2:3]
	v_or_b32_e32 v2, 0x200, v0
	v_lshrrev_b32_e32 v2, 5, v2
	v_xor_b32_e32 v9, v2, v0
	v_lshlrev_b32_e32 v9, 4, v9
	v_lshlrev_b32_e32 v8, 9, v2
	v_and_b32_e32 v9, 0x1f0, v9
	v_add3_u32 v8, 0, v8, v9
	ds_read_b128 v[8:11], v8
	v_lshlrev_b32_e32 v2, 11, v2
	s_waitcnt lgkmcnt(1)
	global_store_dwordx4 v[14:15], v[4:7], off sc1
	s_nop 1
	v_lshl_add_u64 v[4:5], v[12:13], 0, v[2:3]
	s_waitcnt lgkmcnt(0)
	global_store_dwordx4 v[4:5], v[8:11], off sc1
	v_or_b32_e32 v2, 32, v1
	v_lshlrev_b32_e32 v4, 9, v2
	v_or_b32_e32 v8, 0x600, v0
	v_lshrrev_b32_e32 v17, 5, v8
	v_xor_b32_e32 v9, v17, v0
	v_lshlrev_b32_e32 v9, 4, v9
	v_add3_u32 v4, 0, v4, v16
	v_lshlrev_b32_e32 v8, 9, v17
	v_and_b32_e32 v9, 0x1f0, v9
	ds_read_b128 v[4:7], v4
	v_add3_u32 v8, 0, v8, v9
	ds_read_b128 v[8:11], v8
	v_lshlrev_b32_e32 v2, 11, v2
	v_lshl_add_u64 v[14:15], v[12:13], 0, v[2:3]
	v_lshlrev_b32_e32 v2, 11, v17
	s_waitcnt lgkmcnt(1)
	global_store_dwordx4 v[14:15], v[4:7], off sc1
	s_nop 1
	v_lshl_add_u64 v[4:5], v[12:13], 0, v[2:3]
	s_waitcnt lgkmcnt(0)
	global_store_dwordx4 v[4:5], v[8:11], off sc1
	v_or_b32_e32 v2, 64, v1
	v_lshlrev_b32_e32 v4, 9, v2
	v_or_b32_e32 v8, 0xa00, v0
	v_lshrrev_b32_e32 v17, 5, v8
	v_xor_b32_e32 v9, v17, v0
	v_lshlrev_b32_e32 v9, 4, v9
	v_add3_u32 v4, 0, v4, v16
	v_lshlrev_b32_e32 v8, 9, v17
	v_and_b32_e32 v9, 0x1f0, v9
	ds_read_b128 v[4:7], v4
	v_add3_u32 v8, 0, v8, v9
	ds_read_b128 v[8:11], v8
	v_lshlrev_b32_e32 v2, 11, v2
	v_lshl_add_u64 v[14:15], v[12:13], 0, v[2:3]
	v_lshlrev_b32_e32 v2, 11, v17
	s_waitcnt lgkmcnt(1)
	global_store_dwordx4 v[14:15], v[4:7], off sc1
	s_nop 1
	v_lshl_add_u64 v[4:5], v[12:13], 0, v[2:3]
	s_waitcnt lgkmcnt(0)
	global_store_dwordx4 v[4:5], v[8:11], off sc1
	v_or_b32_e32 v2, 0x60, v1
	v_lshlrev_b32_e32 v4, 9, v2
	v_or_b32_e32 v8, 0xe00, v0
	v_lshrrev_b32_e32 v17, 5, v8
	v_xor_b32_e32 v9, v17, v0
	v_lshlrev_b32_e32 v9, 4, v9
	v_add3_u32 v4, 0, v4, v16
	v_lshlrev_b32_e32 v8, 9, v17
	v_and_b32_e32 v9, 0x1f0, v9
	ds_read_b128 v[4:7], v4
	v_add3_u32 v8, 0, v8, v9
	ds_read_b128 v[8:11], v8
	v_lshlrev_b32_e32 v2, 11, v2
	v_lshl_add_u64 v[14:15], v[12:13], 0, v[2:3]
	v_lshlrev_b32_e32 v2, 11, v17
	s_waitcnt lgkmcnt(1)
	global_store_dwordx4 v[14:15], v[4:7], off sc1
	s_nop 1
	v_lshl_add_u64 v[4:5], v[12:13], 0, v[2:3]
	s_waitcnt lgkmcnt(0)
	global_store_dwordx4 v[4:5], v[8:11], off sc1
	v_or_b32_e32 v2, 0x80, v1
	v_lshlrev_b32_e32 v4, 9, v2
	v_or_b32_e32 v8, 0x1200, v0
	v_lshrrev_b32_e32 v17, 5, v8
	v_xor_b32_e32 v9, v17, v0
	v_lshlrev_b32_e32 v9, 4, v9
	v_add3_u32 v4, 0, v4, v16
	v_lshlrev_b32_e32 v8, 9, v17
	v_and_b32_e32 v9, 0x1f0, v9
	ds_read_b128 v[4:7], v4
	v_add3_u32 v8, 0, v8, v9
	ds_read_b128 v[8:11], v8
	v_lshlrev_b32_e32 v2, 11, v2
	v_lshl_add_u64 v[14:15], v[12:13], 0, v[2:3]
	v_lshlrev_b32_e32 v2, 11, v17
	s_waitcnt lgkmcnt(1)
	global_store_dwordx4 v[14:15], v[4:7], off sc1
	s_nop 1
	v_lshl_add_u64 v[4:5], v[12:13], 0, v[2:3]
	s_waitcnt lgkmcnt(0)
	global_store_dwordx4 v[4:5], v[8:11], off sc1
	v_or_b32_e32 v2, 0xa0, v1
	v_lshlrev_b32_e32 v4, 9, v2
	v_or_b32_e32 v8, 0x1600, v0
	v_lshrrev_b32_e32 v17, 5, v8
	v_xor_b32_e32 v9, v17, v0
	v_lshlrev_b32_e32 v9, 4, v9
	v_add3_u32 v4, 0, v4, v16
	v_lshlrev_b32_e32 v8, 9, v17
	v_and_b32_e32 v9, 0x1f0, v9
	ds_read_b128 v[4:7], v4
	v_add3_u32 v8, 0, v8, v9
	ds_read_b128 v[8:11], v8
	v_lshlrev_b32_e32 v2, 11, v2
	v_lshl_add_u64 v[14:15], v[12:13], 0, v[2:3]
	v_lshlrev_b32_e32 v2, 11, v17
	s_waitcnt lgkmcnt(1)
	global_store_dwordx4 v[14:15], v[4:7], off sc1
	s_nop 1
	v_lshl_add_u64 v[4:5], v[12:13], 0, v[2:3]
	s_waitcnt lgkmcnt(0)
	global_store_dwordx4 v[4:5], v[8:11], off sc1
	v_or_b32_e32 v2, 0xc0, v1
	v_lshlrev_b32_e32 v4, 9, v2
	v_or_b32_e32 v8, 0x1a00, v0
	v_lshrrev_b32_e32 v17, 5, v8
	v_xor_b32_e32 v9, v17, v0
	v_add3_u32 v4, 0, v4, v16
	v_lshlrev_b32_e32 v9, 4, v9
	ds_read_b128 v[4:7], v4
	v_lshlrev_b32_e32 v8, 9, v17
	v_and_b32_e32 v9, 0x1f0, v9
	v_add3_u32 v8, 0, v8, v9
	ds_read_b128 v[8:11], v8
	v_lshlrev_b32_e32 v2, 11, v2
	v_lshl_add_u64 v[14:15], v[12:13], 0, v[2:3]
	v_lshlrev_b32_e32 v2, 11, v17
	v_or_b32_e32 v1, 0xe0, v1
	s_waitcnt lgkmcnt(1)
	global_store_dwordx4 v[14:15], v[4:7], off sc1
	s_nop 1
	v_lshl_add_u64 v[4:5], v[12:13], 0, v[2:3]
	v_lshlrev_b32_e32 v2, 9, v1
	v_add3_u32 v2, 0, v2, v16
	s_waitcnt lgkmcnt(0)
	global_store_dwordx4 v[4:5], v[8:11], off sc1
	ds_read_b128 v[4:7], v2
	v_lshlrev_b32_e32 v2, 11, v1
	v_or_b32_e32 v1, 0x1e00, v0
	v_lshrrev_b32_e32 v1, 5, v1
	v_xor_b32_e32 v9, v1, v0
	v_lshlrev_b32_e32 v9, 4, v9
	v_lshlrev_b32_e32 v8, 9, v1
	v_and_b32_e32 v9, 0x1f0, v9
	v_add3_u32 v8, 0, v8, v9
	ds_read_b128 v[8:11], v8
	v_lshl_add_u64 v[14:15], v[12:13], 0, v[2:3]
	v_lshlrev_b32_e32 v2, 11, v1
	s_waitcnt lgkmcnt(1)
	global_store_dwordx4 v[14:15], v[4:7], off sc1
	s_nop 1
	v_lshl_add_u64 v[4:5], v[12:13], 0, v[2:3]
	s_waitcnt lgkmcnt(0)
	global_store_dwordx4 v[4:5], v[8:11], off sc1
	s_waitcnt lgkmcnt(0)
	s_barrier
	s_lshl_b32 s3, s2, 3
	s_and_b32 s3, s3, 56
	s_ashr_i32 s17, s2, 5
	s_add_i32 s20, s3, s17
	s_ashr_i32 s21, s20, 31
	s_bfe_u32 s16, s2, 0x20003
	s_lshl_b64 s[4:5], s[20:21], 17
	s_lshl_b64 s[6:7], s[20:21], 19
	s_add_u32 s6, s12, s6
	s_addc_u32 s7, s13, s7
	s_lshl_b32 s3, s16, 19
	s_add_u32 s3, s14, s3
	v_ashrrev_i32_e32 v2, 6, v0
	v_lshlrev_b32_e32 v1, 4, v0
	s_addc_u32 s13, s15, 0
	v_lshlrev_b32_e32 v4, 9, v2
	v_and_b32_e32 v5, 0x1f0, v1
	s_add_u32 s12, s3, 0x400000
	v_and_or_b32 v32, v4, s0, v5
	v_lshlrev_b32_e32 v4, 5, v2
	v_and_b32_e32 v5, 48, v1
	s_addc_u32 s13, s13, 0
	v_bitop3_b32 v4, v4, v5, 32 bitop3:0x6c
	s_and_b32 s15, s2, 8
	s_add_i32 s3, s20, 3
	v_bfe_u32 v31, v0, 5, 1
	v_lshrrev_b32_e32 v34, 1, v4
	v_add_u32_e32 v4, s15, v2
	s_mov_b32 s20, 0x3ffffe
	v_and_or_b32 v30, v4, s20, v31
	v_bfe_i32 v5, v30, 0, 22
	v_bfe_u32 v4, v30, 21, 1
	v_add_u32_e32 v6, v5, v4
	v_lshlrev_b32_e32 v4, 3, v6
	v_and_b32_e32 v6, 0x7fffffe, v6
	s_lshl_b32 s0, s17, 4
	v_sub_u32_e32 v5, v5, v6
	s_and_b32 s17, s0, 16
	v_lshl_or_b32 v6, v5, 5, v34
	v_add_u32_e32 v5, s17, v2
	v_and_or_b32 v35, v5, s20, v31
	v_bfe_i32 v7, v35, 0, 22
	v_bfe_u32 v8, v35, 21, 1
	v_add_u32_e32 v8, v7, v8
	v_lshlrev_b32_e32 v9, 3, v8
	v_and_b32_e32 v8, 0x7fffffe, v8
	v_add_u32_e32 v5, 8, v5
	v_sub_u32_e32 v7, v7, v8
	v_and_or_b32 v36, v5, s20, v31
	v_lshl_or_b32 v98, v7, 5, v34
	v_bfe_i32 v5, v36, 0, 22
	v_bfe_u32 v7, v36, 21, 1
	v_add_u32_e32 v7, v5, v7
	v_lshrrev_b32_e32 v33, 6, v32
	v_lshlrev_b32_e32 v8, 3, v7
	v_and_b32_e32 v7, 0x7fffffe, v7
	s_and_b32 s3, s3, 15
	v_and_or_b32 v4, v4, -16, v33
	v_sub_u32_e32 v5, v5, v7
	v_and_or_b32 v14, v9, -16, v33
	v_lshl_or_b32 v100, v5, 5, v34
	v_ashrrev_i32_e32 v5, 31, v4
	s_lshl_b32 s14, s3, 6
	s_lshl_b32 s0, s3, 8
	s_lshl_b32 s2, s3, 7
	v_and_or_b32 v16, v8, -16, v33
	v_lshlrev_b64 v[4:5], 12, v[4:5]
	s_add_u32 s2, s12, s2
	v_ashrrev_i32_e32 v15, 31, v14
	v_lshl_add_u64 v[4:5], s[6:7], 0, v[4:5]
	v_ashrrev_i32_e32 v7, 31, v6
	s_addc_u32 s3, s13, 0
	v_lshlrev_b64 v[102:103], 11, v[14:15]
	v_ashrrev_i32_e32 v99, 31, v98
	v_ashrrev_i32_e32 v17, 31, v16
	v_lshl_add_u64 v[8:9], v[4:5], 0, s[0:1]
	v_lshlrev_b64 v[38:39], 2, v[6:7]
	v_lshl_add_u64 v[14:15], s[2:3], 0, v[102:103]
	v_lshlrev_b64 v[22:23], 1, v[98:99]
	v_lshlrev_b64 v[104:105], 11, v[16:17]
	v_ashrrev_i32_e32 v101, 31, v100
	v_lshl_add_u64 v[18:19], v[8:9], 0, v[38:39]
	v_lshl_add_u64 v[24:25], v[14:15], 0, v[22:23]
	v_lshl_add_u64 v[14:15], s[2:3], 0, v[104:105]
	v_lshlrev_b64 v[26:27], 1, v[100:101]
	global_load_dwordx4 v[6:9], v[18:19], off offset:16
	global_load_dwordx4 v[10:13], v[18:19], off
	v_lshl_add_u64 v[28:29], v[14:15], 0, v[26:27]
	global_load_dwordx4 v[14:17], v[24:25], off
	global_load_dwordx4 v[18:21], v[28:29], off
	v_lshlrev_b32_e32 v24, 10, v30
	v_or_b32_e32 v125, v24, v32
	v_xad_u32 v24, s15, 8, v2
	v_and_or_b32 v24, v24, s20, v31
	v_lshlrev_b32_e32 v25, 10, v24
	v_or_b32_e32 v122, v25, v32
	v_bfe_i32 v25, v24, 0, 22
	v_bfe_u32 v24, v24, 21, 1
	v_add_u32_e32 v28, v25, v24
	v_lshlrev_b32_e32 v24, 3, v28
	v_and_b32_e32 v28, 0x7fffffe, v28
	v_sub_u32_e32 v25, v25, v28
	v_lshl_or_b32 v28, v25, 5, v34
	v_lshlrev_b32_e32 v25, 10, v35
	v_or_b32_e32 v126, v25, v32
	v_lshlrev_b32_e32 v25, 10, v36
	v_or_b32_e32 v127, v25, v32
	v_xad_u32 v25, s17, 16, v2
	v_and_or_b32 v25, v25, s20, v31
	v_lshlrev_b32_e32 v29, 10, v25
	v_or_b32_e32 v123, v29, v32
	v_bfe_i32 v29, v25, 0, 22
	v_bfe_u32 v25, v25, 21, 1
	v_add_u32_e32 v25, v29, v25
	v_and_b32_e32 v121, 3, v2
	v_lshlrev_b32_e32 v30, 3, v25
	v_and_b32_e32 v25, 0x7fffffe, v25
	v_xad_u32 v2, s17, 24, v2
	v_sub_u32_e32 v25, v29, v25
	v_and_or_b32 v2, v2, s20, v31
	v_lshl_or_b32 v106, v25, 5, v34
	v_lshlrev_b32_e32 v25, 10, v2
	v_or_b32_e32 v124, v25, v32
	v_bfe_i32 v25, v2, 0, 22
	v_bfe_u32 v2, v2, 21, 1
	v_add_u32_e32 v2, v25, v2
	v_lshlrev_b32_e32 v29, 3, v2
	v_and_b32_e32 v2, 0x7fffffe, v2
	v_and_b32_e32 v118, 15, v0
	v_sub_u32_e32 v2, v25, v2
	v_lshlrev_b32_e32 v25, 2, v0
	v_ashrrev_i32_e32 v120, 8, v0
	v_and_or_b32 v32, v29, -16, v33
	v_lshl_or_b32 v108, v2, 5, v34
	v_and_b32_e32 v2, 48, v0
	v_and_b32_e32 v25, 32, v25
	v_lshlrev_b32_e32 v29, 6, v118
	v_and_b32_e32 v119, 63, v0
	v_and_or_b32 v24, v24, -16, v33
	v_and_or_b32 v30, v30, -16, v33
	v_lshlrev_b32_e32 v68, 13, v120
	v_bitop3_b32 v2, v29, v25, v2 bitop3:0x36
	v_ashrrev_i32_e32 v25, 31, v24
	v_lshlrev_b64 v[24:25], 12, v[24:25]
	v_lshl_add_u64 v[56:57], s[6:7], 0, v[24:25]
	v_ashrrev_i32_e32 v29, 31, v28
	v_lshl_add_u64 v[24:25], v[56:57], 0, s[0:1]
	v_lshlrev_b64 v[58:59], 2, v[28:29]
	v_ashrrev_i32_e32 v31, 31, v30
	v_lshl_add_u64 v[24:25], v[24:25], 0, v[58:59]
	v_lshlrev_b64 v[110:111], 11, v[30:31]
	v_ashrrev_i32_e32 v107, 31, v106
	v_ashrrev_i32_e32 v33, 31, v32
	global_load_dwordx4 v[40:43], v[24:25], off offset:16
	global_load_dwordx4 v[44:47], v[24:25], off
	v_lshl_add_u64 v[24:25], s[2:3], 0, v[110:111]
	v_lshlrev_b64 v[60:61], 1, v[106:107]
	v_lshlrev_b64 v[112:113], 11, v[32:33]
	v_ashrrev_i32_e32 v109, 31, v108
	v_lshl_add_u64 v[24:25], v[24:25], 0, v[60:61]
	v_lshl_add_u64 v[28:29], s[2:3], 0, v[112:113]
	v_lshlrev_b64 v[62:63], 1, v[108:109]
	v_lshl_add_u64 v[28:29], v[28:29], 0, v[62:63]
	global_load_dwordx4 v[48:51], v[24:25], off
	global_load_dwordx4 v[52:55], v[28:29], off
	s_add_i32 s0, s14, 64
	s_and_b32 s2, s0, 0x3c0
	s_lshl_b32 s0, s2, 2
	s_lshl_b32 s2, s2, 1
	v_lshl_add_u64 v[24:25], v[4:5], 0, s[0:1]
	s_add_u32 s2, s12, s2
	v_lshl_add_u64 v[24:25], v[24:25], 0, v[38:39]
	s_addc_u32 s3, s13, 0
	global_load_dwordx4 v[30:33], v[24:25], off offset:16
	global_load_dwordx4 v[34:37], v[24:25], off
	v_lshl_add_u64 v[24:25], s[2:3], 0, v[102:103]
	v_lshl_add_u64 v[64:65], v[24:25], 0, v[22:23]
	v_lshl_add_u64 v[22:23], s[2:3], 0, v[104:105]
	v_lshl_add_u64 v[66:67], v[22:23], 0, v[26:27]
	global_load_dwordx4 v[26:29], v[64:65], off
	global_load_dwordx4 v[22:25], v[66:67], off
	v_add_u32_e32 v64, 0, v125
	s_waitcnt vmcnt(10)
	v_cvt_pk_bf16_f32 v10, v10, v11
	v_cvt_pk_bf16_f32 v11, v12, v13
	v_cvt_pk_bf16_f32 v12, v6, v7
	v_add_u32_e32 v6, 0, v126
	v_cvt_pk_bf16_f32 v13, v8, v9
	ds_write_b128 v64, v[10:13]
	s_waitcnt vmcnt(9)
	ds_write_b128 v6, v[14:17] offset:32768
	v_add_u32_e32 v6, 0, v127
	s_waitcnt vmcnt(8)
	ds_write_b128 v6, v[18:21] offset:32768
	v_add_u32_e32 v10, 0, v122
	s_waitcnt vmcnt(6)
	v_cvt_pk_bf16_f32 v6, v44, v45
	v_cvt_pk_bf16_f32 v7, v46, v47
	v_cvt_pk_bf16_f32 v8, v40, v41
	v_cvt_pk_bf16_f32 v9, v42, v43
	ds_write_b128 v10, v[6:9]
	v_add_u32_e32 v6, 0, v123
	s_waitcnt vmcnt(5)
	ds_write_b128 v6, v[48:51] offset:32768
	v_add_u32_e32 v6, 0, v124
	s_waitcnt vmcnt(4)
	ds_write_b128 v6, v[52:55] offset:32768
	v_lshl_add_u64 v[6:7], v[56:57], 0, s[0:1]
	v_lshl_add_u64 v[14:15], v[6:7], 0, v[58:59]
	global_load_dwordx4 v[6:9], v[14:15], off offset:16
	global_load_dwordx4 v[10:13], v[14:15], off
	v_lshl_add_u64 v[14:15], s[2:3], 0, v[110:111]
	v_lshl_add_u64 v[40:41], v[14:15], 0, v[60:61]
	v_lshl_add_u64 v[14:15], s[2:3], 0, v[112:113]
	v_lshl_add_u64 v[42:43], v[14:15], 0, v[62:63]
	global_load_dwordx4 v[18:21], v[40:41], off
	global_load_dwordx4 v[14:17], v[42:43], off
	v_lshlrev_b32_e32 v40, 13, v121
	s_cmp_lg_u32 0, -1
	s_waitcnt lgkmcnt(0)
	s_cselect_b32 s0, 0, 0
	v_add3_u32 v128, v68, s0, v2
	s_add_i32 s0, s0, 0x8000
	v_add3_u32 v129, v40, s0, v2
	v_lshl_add_u64 v[114:115], v[4:5], 0, v[38:39]
	v_lshl_add_u64 v[116:117], v[56:57], 0, v[58:59]
	s_add_i32 s2, s14, 0x80
	s_mov_b32 s3, 0
	v_mov_b32_e32 v2, v3
	v_mov_b32_e32 v4, v3
	v_mov_b32_e32 v5, v3
	v_mov_b32_e32 v38, v3
	v_mov_b32_e32 v39, v3
	v_mov_b32_e32 v40, v3
	v_mov_b32_e32 v41, v3
	v_mov_b32_e32 v42, v3
	v_mov_b32_e32 v43, v3
	v_mov_b32_e32 v44, v3
	v_mov_b32_e32 v45, v3
	v_mov_b32_e32 v46, v3
	v_mov_b32_e32 v47, v3
	v_mov_b32_e32 v48, v3
	v_mov_b32_e32 v49, v3
	v_mov_b32_e32 v50, v3
	v_mov_b32_e32 v51, v3
	v_mov_b32_e32 v52, v3
	v_mov_b32_e32 v53, v3
	v_mov_b32_e32 v54, v3
	v_mov_b32_e32 v55, v3
	v_mov_b32_e32 v56, v3
	v_mov_b32_e32 v57, v3
	v_mov_b32_e32 v58, v3
	v_mov_b32_e32 v59, v3
	v_mov_b32_e32 v60, v3
	v_mov_b32_e32 v61, v3
	v_mov_b32_e32 v62, v3
	v_mov_b32_e32 v63, v3
	v_mov_b32_e32 v64, v3
	v_mov_b32_e32 v65, v3
	v_mov_b32_e32 v66, v3
	v_mov_b32_e32 v67, v3
	v_mov_b32_e32 v68, v3
	v_mov_b32_e32 v69, v3
	v_mov_b32_e32 v70, v3
	v_mov_b32_e32 v71, v3
	v_mov_b32_e32 v72, v3
	v_mov_b32_e32 v73, v3
	v_mov_b32_e32 v74, v3
	v_mov_b32_e32 v75, v3
	v_mov_b32_e32 v76, v3
	v_mov_b32_e32 v77, v3
	v_mov_b32_e32 v78, v3
	v_mov_b32_e32 v79, v3
	v_mov_b32_e32 v80, v3
	v_mov_b32_e32 v81, v3
	v_mov_b32_e32 v82, v3
	v_mov_b32_e32 v83, v3
	v_mov_b32_e32 v84, v3
	v_mov_b32_e32 v85, v3
	v_mov_b32_e32 v86, v3
	v_mov_b32_e32 v87, v3
	v_mov_b32_e32 v88, v3
	v_mov_b32_e32 v89, v3
	v_mov_b32_e32 v90, v3
	v_mov_b32_e32 v91, v3
	v_mov_b32_e32 v92, v3
	v_mov_b32_e32 v93, v3
	v_mov_b32_e32 v94, v3
	v_mov_b32_e32 v95, v3
	v_mov_b32_e32 v96, v3
	v_mov_b32_e32 v97, v3
	s_barrier
.LBB1_3:
	s_and_b32 s0, s3, 0x10000
	v_add_u32_e32 v158, s0, v128
	v_add_u32_e32 v159, s0, v129
	ds_read_b128 v[130:133], v159 offset:0
	ds_read_b128 v[134:137], v159 offset:0x800
	ds_read_b128 v[138:141], v159 offset:0x1000
	ds_read_b128 v[142:145], v159 offset:0x1800
	ds_read_b128 v[146:149], v158 offset:0
	ds_read_b128 v[150:153], v158 offset:0x800
	ds_read_b128 v[154:157], v158 offset:0x1000
	s_nop 0
	s_waitcnt lgkmcnt(2)
	s_nop 0
	v_mfma_f32_16x16x32_bf16 v[94:97], v[130:133], v[146:149], v[94:97]
	v_mfma_f32_16x16x32_bf16 v[90:93], v[134:137], v[146:149], v[90:93]
	v_mfma_f32_16x16x32_bf16 v[86:89], v[138:141], v[146:149], v[86:89]
	v_mfma_f32_16x16x32_bf16 v[82:85], v[142:145], v[146:149], v[82:85]
	ds_read_b128 v[146:149], v158 offset:0x1800
	s_waitcnt lgkmcnt(2)
	s_nop 0
	v_mfma_f32_16x16x32_bf16 v[78:81], v[130:133], v[150:153], v[78:81]
	v_mfma_f32_16x16x32_bf16 v[74:77], v[134:137], v[150:153], v[74:77]
	v_mfma_f32_16x16x32_bf16 v[70:73], v[138:141], v[150:153], v[70:73]
	v_mfma_f32_16x16x32_bf16 v[66:69], v[142:145], v[150:153], v[66:69]
	s_waitcnt lgkmcnt(1)
	s_nop 0
	v_mfma_f32_16x16x32_bf16 v[62:65], v[130:133], v[154:157], v[62:65]
	v_mfma_f32_16x16x32_bf16 v[58:61], v[134:137], v[154:157], v[58:61]
	v_mfma_f32_16x16x32_bf16 v[54:57], v[138:141], v[154:157], v[54:57]
	v_mfma_f32_16x16x32_bf16 v[50:53], v[142:145], v[154:157], v[50:53]
	s_waitcnt lgkmcnt(0)
	s_nop 0
	v_mfma_f32_16x16x32_bf16 v[46:49], v[130:133], v[146:149], v[46:49]
	v_mfma_f32_16x16x32_bf16 v[42:45], v[134:137], v[146:149], v[42:45]
	v_mfma_f32_16x16x32_bf16 v[38:41], v[138:141], v[146:149], v[38:41]
	v_mfma_f32_16x16x32_bf16 v[2:5], v[142:145], v[146:149], v[2:5]
	s_xor_b32 s0, s0, 0x10000
	s_and_b32 s6, s2, 0x3c0
	s_add_i32 s14, s0, 0
	s_lshl_b32 s0, s6, 2
	s_lshl_b32 s6, s6, 1
	s_add_u32 s6, s12, s6
	s_waitcnt vmcnt(6)
	v_cvt_pk_bf16_f32 v34, v34, v35
	v_cvt_pk_bf16_f32 v35, v36, v37
	v_cvt_pk_bf16_f32 v36, v30, v31
	v_cvt_pk_bf16_f32 v37, v32, v33
	v_add_u32_e32 v30, s14, v125
	s_addc_u32 s7, s13, 0
	v_add_u32_e32 v31, s14, v126
	v_add_u32_e32 v32, s14, v127
	ds_write_b128 v30, v[34:37]
	s_waitcnt vmcnt(5)
	ds_write_b128 v31, v[26:29] offset:32768
	s_waitcnt vmcnt(4)
	ds_write_b128 v32, v[22:25] offset:32768
	v_lshl_add_u64 v[22:23], s[6:7], 0, v[102:103]
	v_lshl_add_u64 v[24:25], s[6:7], 0, v[104:105]
	v_lshl_add_u64 v[130:131], v[114:115], 0, s[0:1]
	v_lshl_add_u64 v[22:23], v[98:99], 1, v[22:23]
	v_lshl_add_u64 v[24:25], v[100:101], 1, v[24:25]
	global_load_dwordx4 v[30:33], v[130:131], off offset:16
	global_load_dwordx4 v[34:37], v[130:131], off
	global_load_dwordx4 v[26:29], v[22:23], off
	s_nop 0
	global_load_dwordx4 v[22:25], v[24:25], off
	ds_read_b128 v[130:133], v159 offset:0x400
	ds_read_b128 v[134:137], v159 offset:0xc00
	ds_read_b128 v[138:141], v159 offset:0x1400
	ds_read_b128 v[142:145], v159 offset:0x1c00
	ds_read_b128 v[146:149], v158 offset:0x400
	ds_read_b128 v[150:153], v158 offset:0xc00
	ds_read_b128 v[154:157], v158 offset:0x1400
	s_nop 0
	s_waitcnt lgkmcnt(2)
	s_nop 0
	v_mfma_f32_16x16x32_bf16 v[94:97], v[130:133], v[146:149], v[94:97]
	v_mfma_f32_16x16x32_bf16 v[90:93], v[134:137], v[146:149], v[90:93]
	v_mfma_f32_16x16x32_bf16 v[86:89], v[138:141], v[146:149], v[86:89]
	v_mfma_f32_16x16x32_bf16 v[82:85], v[142:145], v[146:149], v[82:85]
	ds_read_b128 v[146:149], v158 offset:0x1c00
	s_waitcnt lgkmcnt(2)
	s_nop 0
	v_mfma_f32_16x16x32_bf16 v[78:81], v[130:133], v[150:153], v[78:81]
	v_mfma_f32_16x16x32_bf16 v[74:77], v[134:137], v[150:153], v[74:77]
	v_mfma_f32_16x16x32_bf16 v[70:73], v[138:141], v[150:153], v[70:73]
	v_mfma_f32_16x16x32_bf16 v[66:69], v[142:145], v[150:153], v[66:69]
	s_waitcnt lgkmcnt(1)
	s_nop 0
	v_mfma_f32_16x16x32_bf16 v[62:65], v[130:133], v[154:157], v[62:65]
	v_mfma_f32_16x16x32_bf16 v[58:61], v[134:137], v[154:157], v[58:61]
	v_mfma_f32_16x16x32_bf16 v[54:57], v[138:141], v[154:157], v[54:57]
	v_mfma_f32_16x16x32_bf16 v[50:53], v[142:145], v[154:157], v[50:53]
	s_waitcnt lgkmcnt(0)
	s_nop 0
	v_mfma_f32_16x16x32_bf16 v[46:49], v[130:133], v[146:149], v[46:49]
	v_mfma_f32_16x16x32_bf16 v[42:45], v[134:137], v[146:149], v[42:45]
	v_mfma_f32_16x16x32_bf16 v[38:41], v[138:141], v[146:149], v[38:41]
	v_mfma_f32_16x16x32_bf16 v[2:5], v[142:145], v[146:149], v[2:5]
	v_add_u32_e32 v130, s14, v122
	s_waitcnt vmcnt(6)
	v_cvt_pk_bf16_f32 v10, v10, v11
	v_cvt_pk_bf16_f32 v11, v12, v13
	v_cvt_pk_bf16_f32 v12, v6, v7
	v_add_u32_e32 v6, s14, v123
	v_cvt_pk_bf16_f32 v13, v8, v9
	ds_write_b128 v130, v[10:13]
	s_waitcnt vmcnt(5)
	ds_write_b128 v6, v[18:21] offset:32768
	v_add_u32_e32 v6, s14, v124
	s_waitcnt vmcnt(4)
	ds_write_b128 v6, v[14:17] offset:32768
	v_lshl_add_u64 v[14:15], s[6:7], 0, v[110:111]
	v_lshl_add_u64 v[16:17], s[6:7], 0, v[112:113]
	v_lshl_add_u64 v[10:11], v[116:117], 0, s[0:1]
	v_lshl_add_u64 v[14:15], v[106:107], 1, v[14:15]
	v_lshl_add_u64 v[16:17], v[108:109], 1, v[16:17]
	global_load_dwordx4 v[6:9], v[10:11], off offset:16
	s_nop 0
	global_load_dwordx4 v[10:13], v[10:11], off
	s_nop 0
	global_load_dwordx4 v[18:21], v[14:15], off
	s_nop 0
	global_load_dwordx4 v[14:17], v[16:17], off
	s_waitcnt lgkmcnt(0)
	s_add_i32 s2, s2, 64
	s_add_i32 s3, s3, 0x10000
	s_cmp_lg_u32 s3, 0xe0000
	s_barrier
	s_cbranch_scc1 .LBB1_3
	ds_read_b128 v[98:101], v129 offset:0
	ds_read_b128 v[102:105], v129 offset:0x800
	ds_read_b128 v[106:109], v129 offset:0x1000
	ds_read_b128 v[110:113], v129 offset:0x1800
	ds_read_b128 v[114:117], v128 offset:0
	ds_read_b128 v[130:133], v128 offset:0x800
	ds_read_b128 v[134:137], v128 offset:0x1000
	s_nop 0
	s_waitcnt lgkmcnt(2)
	s_nop 0
	v_mfma_f32_16x16x32_bf16 v[94:97], v[98:101], v[114:117], v[94:97]
	v_mfma_f32_16x16x32_bf16 v[90:93], v[102:105], v[114:117], v[90:93]
	v_mfma_f32_16x16x32_bf16 v[86:89], v[106:109], v[114:117], v[86:89]
	v_mfma_f32_16x16x32_bf16 v[82:85], v[110:113], v[114:117], v[82:85]
	ds_read_b128 v[114:117], v128 offset:0x1800
	s_waitcnt lgkmcnt(2)
	s_nop 0
	v_mfma_f32_16x16x32_bf16 v[78:81], v[98:101], v[130:133], v[78:81]
	v_mfma_f32_16x16x32_bf16 v[74:77], v[102:105], v[130:133], v[74:77]
	v_mfma_f32_16x16x32_bf16 v[70:73], v[106:109], v[130:133], v[70:73]
	v_mfma_f32_16x16x32_bf16 v[66:69], v[110:113], v[130:133], v[66:69]
	s_waitcnt lgkmcnt(1)
	s_nop 0
	v_mfma_f32_16x16x32_bf16 v[62:65], v[98:101], v[134:137], v[62:65]
	v_mfma_f32_16x16x32_bf16 v[58:61], v[102:105], v[134:137], v[58:61]
	v_mfma_f32_16x16x32_bf16 v[54:57], v[106:109], v[134:137], v[54:57]
	v_mfma_f32_16x16x32_bf16 v[50:53], v[110:113], v[134:137], v[50:53]
	s_waitcnt lgkmcnt(0)
	s_nop 0
	v_mfma_f32_16x16x32_bf16 v[46:49], v[98:101], v[114:117], v[46:49]
	v_mfma_f32_16x16x32_bf16 v[42:45], v[102:105], v[114:117], v[42:45]
	v_mfma_f32_16x16x32_bf16 v[38:41], v[106:109], v[114:117], v[38:41]
	v_mfma_f32_16x16x32_bf16 v[2:5], v[110:113], v[114:117], v[2:5]
	v_add_u32_e32 v98, s18, v125
	s_waitcnt vmcnt(6)
	v_cvt_pk_bf16_f32 v34, v34, v35
	v_cvt_pk_bf16_f32 v35, v36, v37
	v_cvt_pk_bf16_f32 v36, v30, v31
	v_add_u32_e32 v30, s19, v126
	v_cvt_pk_bf16_f32 v37, v32, v33
	ds_write_b128 v98, v[34:37]
	s_waitcnt vmcnt(5)
	ds_write_b128 v30, v[26:29]
	v_add_u32_e32 v26, s19, v127
	s_waitcnt vmcnt(4)
	ds_write_b128 v26, v[22:25]
	ds_read_b128 v[22:25], v129 offset:0x400
	ds_read_b128 v[26:29], v129 offset:0xc00
	ds_read_b128 v[30:33], v129 offset:0x1400
	ds_read_b128 v[34:37], v129 offset:0x1c00
	ds_read_b128 v[98:101], v128 offset:0x400
	ds_read_b128 v[102:105], v128 offset:0xc00
	ds_read_b128 v[106:109], v128 offset:0x1400
	s_nop 0
	s_waitcnt lgkmcnt(2)
	s_nop 0
	v_mfma_f32_16x16x32_bf16 v[94:97], v[22:25], v[98:101], v[94:97]
	v_mfma_f32_16x16x32_bf16 v[90:93], v[26:29], v[98:101], v[90:93]
	v_mfma_f32_16x16x32_bf16 v[86:89], v[30:33], v[98:101], v[86:89]
	v_mfma_f32_16x16x32_bf16 v[82:85], v[34:37], v[98:101], v[82:85]
	ds_read_b128 v[98:101], v128 offset:0x1c00
	s_waitcnt lgkmcnt(2)
	s_nop 0
	v_mfma_f32_16x16x32_bf16 v[78:81], v[22:25], v[102:105], v[78:81]
	v_mfma_f32_16x16x32_bf16 v[74:77], v[26:29], v[102:105], v[74:77]
	v_mfma_f32_16x16x32_bf16 v[70:73], v[30:33], v[102:105], v[70:73]
	v_mfma_f32_16x16x32_bf16 v[66:69], v[34:37], v[102:105], v[66:69]
	s_waitcnt lgkmcnt(1)
	s_nop 0
	v_mfma_f32_16x16x32_bf16 v[62:65], v[22:25], v[106:109], v[62:65]
	v_mfma_f32_16x16x32_bf16 v[58:61], v[26:29], v[106:109], v[58:61]
	v_mfma_f32_16x16x32_bf16 v[54:57], v[30:33], v[106:109], v[54:57]
	v_mfma_f32_16x16x32_bf16 v[50:53], v[34:37], v[106:109], v[50:53]
	s_waitcnt lgkmcnt(0)
	s_nop 0
	v_mfma_f32_16x16x32_bf16 v[22:25], v[22:25], v[98:101], v[46:49]
	v_mfma_f32_16x16x32_bf16 v[26:29], v[26:29], v[98:101], v[42:45]
	v_mfma_f32_16x16x32_bf16 v[30:33], v[30:33], v[98:101], v[38:41]
	v_mfma_f32_16x16x32_bf16 v[2:5], v[34:37], v[98:101], v[2:5]
	v_add_u32_e32 v34, s18, v122
	s_waitcnt vmcnt(2)
	v_cvt_pk_bf16_f32 v10, v10, v11
	v_cvt_pk_bf16_f32 v11, v12, v13
	v_cvt_pk_bf16_f32 v12, v6, v7
	v_add_u32_e32 v6, s19, v123
	s_lshl_b64 s[0:1], s[4:5], 1
	v_cvt_pk_bf16_f32 v13, v8, v9
	ds_write_b128 v34, v[10:13]
	s_waitcnt vmcnt(1)
	ds_write_b128 v6, v[18:21]
	v_add_u32_e32 v6, s19, v124
	s_add_u32 s0, s10, s0
	s_waitcnt vmcnt(0)
	ds_write_b128 v6, v[14:17]
	s_addc_u32 s1, s11, s1
	s_lshl_b32 s2, s16, 9
	s_waitcnt lgkmcnt(0)
	s_barrier
	v_add_u32_e32 v110, 0x10000, v128
	v_add_u32_e32 v102, 0x10000, v129
	ds_read_b128 v[6:9], v102 offset:0
	ds_read_b128 v[10:13], v102 offset:0x800
	ds_read_b128 v[14:17], v102 offset:0x1000
	ds_read_b128 v[18:21], v102 offset:0x1800
	ds_read_b128 v[34:37], v110 offset:0
	ds_read_b128 v[38:41], v110 offset:0x800
	ds_read_b128 v[42:45], v110 offset:0x1000
	s_add_u32 s0, s0, s2
	s_addc_u32 s1, s1, 0
	s_lshl_b32 s2, s16, 10
	s_waitcnt lgkmcnt(2)
	s_add_u32 s2, s8, s2
	v_mfma_f32_16x16x32_bf16 v[46:49], v[6:9], v[34:37], v[94:97]
	s_addc_u32 s3, s9, 0
	v_mfma_f32_16x16x32_bf16 v[90:93], v[10:13], v[34:37], v[90:93]
	v_mfma_f32_16x16x32_bf16 v[86:89], v[14:17], v[34:37], v[86:89]
	v_mfma_f32_16x16x32_bf16 v[34:37], v[18:21], v[34:37], v[82:85]
	ds_read_b128 v[82:85], v110 offset:0x1800
	s_waitcnt lgkmcnt(2)
	s_nop 0
	v_mfma_f32_16x16x32_bf16 v[78:81], v[6:9], v[38:41], v[78:81]
	v_mfma_f32_16x16x32_bf16 v[74:77], v[10:13], v[38:41], v[74:77]
	v_mfma_f32_16x16x32_bf16 v[70:73], v[14:17], v[38:41], v[70:73]
	v_mfma_f32_16x16x32_bf16 v[38:41], v[18:21], v[38:41], v[66:69]
	s_waitcnt lgkmcnt(1)
	s_nop 0
	v_mfma_f32_16x16x32_bf16 v[62:65], v[6:9], v[42:45], v[62:65]
	v_mfma_f32_16x16x32_bf16 v[58:61], v[10:13], v[42:45], v[58:61]
	v_mfma_f32_16x16x32_bf16 v[54:57], v[14:17], v[42:45], v[54:57]
	v_mfma_f32_16x16x32_bf16 v[42:45], v[18:21], v[42:45], v[50:53]
	s_waitcnt lgkmcnt(0)
	s_nop 0
	v_mfma_f32_16x16x32_bf16 v[50:53], v[6:9], v[82:85], v[22:25]
	v_mfma_f32_16x16x32_bf16 v[66:69], v[10:13], v[82:85], v[26:29]
	v_mfma_f32_16x16x32_bf16 v[94:97], v[14:17], v[82:85], v[30:33]
	v_mfma_f32_16x16x32_bf16 v[2:5], v[18:21], v[82:85], v[2:5]
	ds_read_b128 v[18:21], v102 offset:0x400
	ds_read_b128 v[82:85], v102 offset:0xc00
	ds_read_b128 v[98:101], v102 offset:0x1400
	ds_read_b128 v[102:105], v102 offset:0x1c00
	ds_read_b128 v[6:9], v110 offset:0x400
	ds_read_b128 v[10:13], v110 offset:0xc00
	ds_read_b128 v[106:109], v110 offset:0x1400
	s_nop 0
	s_waitcnt lgkmcnt(2)
	s_nop 0
	v_mfma_f32_16x16x32_bf16 v[46:49], v[18:21], v[6:9], v[46:49]
	v_mfma_f32_16x16x32_bf16 v[90:93], v[82:85], v[6:9], v[90:93]
	v_mfma_f32_16x16x32_bf16 v[30:33], v[98:101], v[6:9], v[86:89]
	v_mfma_f32_16x16x32_bf16 v[14:17], v[102:105], v[6:9], v[34:37]
	ds_read_b128 v[86:89], v110 offset:0x1c00
	s_waitcnt lgkmcnt(2)
	s_nop 0
	v_mfma_f32_16x16x32_bf16 v[78:81], v[18:21], v[10:13], v[78:81]
	v_mfma_f32_16x16x32_bf16 v[74:77], v[82:85], v[10:13], v[74:77]
	v_mfma_f32_16x16x32_bf16 v[26:29], v[98:101], v[10:13], v[70:73]
	v_mfma_f32_16x16x32_bf16 v[10:13], v[102:105], v[10:13], v[38:41]
	s_waitcnt lgkmcnt(1)
	s_nop 0
	v_mfma_f32_16x16x32_bf16 v[62:65], v[18:21], v[106:109], v[62:65]
	v_mfma_f32_16x16x32_bf16 v[38:41], v[82:85], v[106:109], v[58:61]
	v_mfma_f32_16x16x32_bf16 v[22:25], v[98:101], v[106:109], v[54:57]
	v_mfma_f32_16x16x32_bf16 v[6:9], v[102:105], v[106:109], v[42:45]
	s_waitcnt lgkmcnt(0)
	s_nop 0
	v_mfma_f32_16x16x32_bf16 v[42:45], v[18:21], v[86:89], v[50:53]
	v_mfma_f32_16x16x32_bf16 v[34:37], v[82:85], v[86:89], v[66:69]
	v_mfma_f32_16x16x32_bf16 v[18:21], v[98:101], v[86:89], v[94:97]
	v_mfma_f32_16x16x32_bf16 v[2:5], v[102:105], v[86:89], v[2:5]
	v_lshrrev_b32_e32 v50, 2, v119
	v_and_b32_e32 v50, 12, v50
	v_lshl_or_b32 v66, v121, 6, v50
	v_lshlrev_b32_e32 v67, 2, v66
	s_waitcnt lgkmcnt(0)
	s_barrier
	global_load_dwordx4 v[50:53], v67, s[2:3]
	global_load_dwordx4 v[54:57], v67, s[2:3] offset:64
	v_lshrrev_b32_e32 v58, 1, v119
	v_lshl_or_b32 v59, v120, 6, v118
	v_and_b32_e32 v68, 8, v58
	v_lshl_add_u32 v69, v59, 9, 0
	v_or_b32_e32 v70, 16, v59
	v_or_b32_e32 v71, 48, v59
	v_lshrrev_b32_e32 v58, 3, v66
	v_or_b32_e32 v59, 16, v66
	v_bitop3_b32 v83, v70, v58, 31 bitop3:0x6c
	v_lshrrev_b32_e32 v85, 3, v59
	v_lshl_add_u32 v72, v70, 9, 0
	v_xor_b32_e32 v82, v58, v118
	v_bitop3_b32 v84, v71, v58, 31 bitop3:0x6c
	v_lshlrev_b32_e32 v83, 4, v83
	v_xor_b32_e32 v86, v85, v118
	v_lshl_add_u32 v73, v71, 9, 0
	v_lshlrev_b32_e32 v82, 4, v82
	v_lshlrev_b32_e32 v84, 4, v84
	v_add3_u32 v83, v72, v83, v68
	v_lshlrev_b32_e32 v86, 4, v86
	global_load_dwordx4 v[58:61], v67, s[2:3] offset:128
	v_add3_u32 v82, v69, v82, v68
	v_add3_u32 v84, v73, v84, v68
	v_add3_u32 v86, v69, v86, v68
	s_waitcnt vmcnt(2)
	v_add_f32_e32 v46, v46, v50
	v_add_f32_e32 v47, v47, v51
	v_add_f32_e32 v48, v48, v52
	v_add_f32_e32 v49, v49, v53
	v_add_f32_e32 v78, v78, v50
	v_add_f32_e32 v79, v79, v51
	v_add_f32_e32 v80, v80, v52
	v_add_f32_e32 v81, v81, v53
	v_add_f32_e32 v62, v62, v50
	v_add_f32_e32 v63, v63, v51
	v_add_f32_e32 v42, v42, v50
	v_add_f32_e32 v43, v43, v51
	v_add_f32_e32 v44, v44, v52
	v_add_f32_e32 v45, v45, v53
	s_waitcnt vmcnt(1)
	v_add_f32_e32 v50, v90, v54
	v_add_f32_e32 v51, v91, v55
	v_add_f32_e32 v64, v64, v52
	v_add_f32_e32 v65, v65, v53
	v_add_f32_e32 v52, v92, v56
	v_add_f32_e32 v53, v93, v57
	v_max_f32_e32 v46, 0, v46
	v_max_f32_e32 v47, 0, v47
	v_max_f32_e32 v48, 0, v48
	v_max_f32_e32 v49, 0, v49
	v_max_f32_e32 v78, 0, v78
	v_max_f32_e32 v79, 0, v79
	v_max_f32_e32 v80, 0, v80
	v_max_f32_e32 v81, 0, v81
	v_max_f32_e32 v88, 0, v43
	v_max_f32_e32 v89, 0, v44
	v_max_f32_e32 v90, 0, v45
	v_max_f32_e32 v50, 0, v50
	v_max_f32_e32 v51, 0, v51
	v_cvt_pk_bf16_f32 v43, v48, v49
	v_cvt_pk_bf16_f32 v44, v78, v79
	v_cvt_pk_bf16_f32 v45, v80, v81
	v_max_f32_e32 v62, 0, v62
	v_max_f32_e32 v63, 0, v63
	v_max_f32_e32 v64, 0, v64
	v_max_f32_e32 v65, 0, v65
	v_max_f32_e32 v87, 0, v42
	v_max_f32_e32 v52, 0, v52
	v_max_f32_e32 v53, 0, v53
	v_cvt_pk_bf16_f32 v42, v46, v47
	v_cvt_pk_bf16_f32 v46, v62, v63
	v_cvt_pk_bf16_f32 v47, v64, v65
	v_cvt_pk_bf16_f32 v48, v87, v88
	v_cvt_pk_bf16_f32 v49, v89, v90
	v_cvt_pk_bf16_f32 v50, v50, v51
	v_cvt_pk_bf16_f32 v51, v52, v53
	ds_write_b64 v83, v[44:45]
	ds_write2st64_b64 v82, v[42:43], v[46:47] offset1:32
	ds_write_b64 v84, v[48:49]
	ds_write_b64 v86, v[50:51]
	v_add_f32_e32 v43, v76, v56
	v_add_f32_e32 v44, v77, v57
	v_max_f32_e32 v43, 0, v43
	v_max_f32_e32 v44, 0, v44
	v_add_f32_e32 v42, v75, v55
	v_cvt_pk_bf16_f32 v43, v43, v44
	v_bitop3_b32 v44, v85, v70, 31 bitop3:0x78
	v_add_f32_e32 v74, v74, v54
	v_max_f32_e32 v42, 0, v42
	v_lshlrev_b32_e32 v44, 4, v44
	v_max_f32_e32 v74, 0, v74
	v_cvt_pk_bf16_f32 v42, v74, v42
	v_add3_u32 v44, v72, v44, v68
	ds_write_b64 v44, v[42:43]
	global_load_dwordx4 v[42:45], v67, s[2:3] offset:192
	v_add_f32_e32 v34, v34, v54
	v_add_f32_e32 v35, v35, v55
	v_add_f32_e32 v36, v36, v56
	v_max_f32_e32 v34, 0, v34
	v_max_f32_e32 v35, 0, v35
	v_max_f32_e32 v36, 0, v36
	v_add_f32_e32 v37, v37, v57
	v_max_f32_e32 v37, 0, v37
	v_cvt_pk_bf16_f32 v34, v34, v35
	v_cvt_pk_bf16_f32 v35, v36, v37
	v_bitop3_b32 v36, v85, v71, 31 bitop3:0x78
	v_add_f32_e32 v38, v38, v54
	v_add_f32_e32 v39, v39, v55
	v_lshlrev_b32_e32 v36, 4, v36
	v_max_f32_e32 v38, 0, v38
	v_max_f32_e32 v39, 0, v39
	v_add_f32_e32 v40, v40, v56
	v_add_f32_e32 v41, v41, v57
	v_add3_u32 v36, v73, v36, v68
	v_max_f32_e32 v40, 0, v40
	v_max_f32_e32 v41, 0, v41
	v_cvt_pk_bf16_f32 v38, v38, v39
	v_cvt_pk_bf16_f32 v39, v40, v41
	ds_write_b64 v86, v[38:39] offset:16384
	ds_write_b64 v36, v[34:35]
	v_or_b32_e32 v34, 32, v66
	s_waitcnt vmcnt(1)
	v_add_f32_e32 v30, v30, v58
	v_add_f32_e32 v31, v31, v59
	v_add_f32_e32 v32, v32, v60
	v_add_f32_e32 v26, v26, v58
	v_add_f32_e32 v27, v27, v59
	v_add_f32_e32 v28, v28, v60
	v_add_f32_e32 v18, v18, v58
	v_add_f32_e32 v19, v19, v59
	v_add_f32_e32 v20, v20, v60
	v_lshrrev_b32_e32 v34, 3, v34
	v_max_f32_e32 v30, 0, v30
	v_max_f32_e32 v31, 0, v31
	v_max_f32_e32 v32, 0, v32
	v_add_f32_e32 v33, v33, v61
	v_max_f32_e32 v26, 0, v26
	v_max_f32_e32 v27, 0, v27
	v_max_f32_e32 v28, 0, v28
	v_add_f32_e32 v29, v29, v61
	v_max_f32_e32 v18, 0, v18
	v_max_f32_e32 v19, 0, v19
	v_max_f32_e32 v20, 0, v20
	v_add_f32_e32 v21, v21, v61
	v_max_f32_e32 v33, 0, v33
	v_cvt_pk_bf16_f32 v30, v30, v31
	v_cvt_pk_bf16_f32 v31, v32, v33
	v_xor_b32_e32 v32, v34, v118
	v_max_f32_e32 v29, 0, v29
	v_cvt_pk_bf16_f32 v26, v26, v27
	v_cvt_pk_bf16_f32 v27, v28, v29
	v_bitop3_b32 v28, v34, v70, 31 bitop3:0x78
	v_max_f32_e32 v21, 0, v21
	v_cvt_pk_bf16_f32 v18, v18, v19
	v_cvt_pk_bf16_f32 v19, v20, v21
	v_bitop3_b32 v20, v34, v71, 31 bitop3:0x78
	v_lshlrev_b32_e32 v32, 4, v32
	v_lshlrev_b32_e32 v28, 4, v28
	v_add_f32_e32 v22, v22, v58
	v_add_f32_e32 v23, v23, v59
	v_lshlrev_b32_e32 v20, 4, v20
	v_add3_u32 v32, v69, v32, v68
	v_add3_u32 v28, v72, v28, v68
	v_max_f32_e32 v22, 0, v22
	v_max_f32_e32 v23, 0, v23
	v_add_f32_e32 v24, v24, v60
	v_add_f32_e32 v25, v25, v61
	v_add3_u32 v20, v73, v20, v68
	ds_write_b64 v32, v[30:31]
	ds_write_b64 v28, v[26:27]
	v_max_f32_e32 v24, 0, v24
	v_max_f32_e32 v25, 0, v25
	v_cvt_pk_bf16_f32 v22, v22, v23
	v_cvt_pk_bf16_f32 v23, v24, v25
	ds_write_b64 v32, v[22:23] offset:16384
	ds_write_b64 v20, v[18:19]
	v_or_b32_e32 v18, 48, v66
	s_waitcnt vmcnt(0)
	v_add_f32_e32 v14, v14, v42
	v_add_f32_e32 v15, v15, v43
	v_add_f32_e32 v16, v16, v44
	v_add_f32_e32 v10, v10, v42
	v_add_f32_e32 v11, v11, v43
	v_add_f32_e32 v12, v12, v44
	v_add_f32_e32 v2, v2, v42
	v_add_f32_e32 v3, v3, v43
	v_add_f32_e32 v4, v4, v44
	v_lshrrev_b32_e32 v18, 3, v18
	v_max_f32_e32 v14, 0, v14
	v_max_f32_e32 v15, 0, v15
	v_max_f32_e32 v16, 0, v16
	v_add_f32_e32 v17, v17, v45
	v_max_f32_e32 v10, 0, v10
	v_max_f32_e32 v11, 0, v11
	v_max_f32_e32 v12, 0, v12
	v_add_f32_e32 v13, v13, v45
	v_max_f32_e32 v2, 0, v2
	v_max_f32_e32 v3, 0, v3
	v_max_f32_e32 v4, 0, v4
	v_add_f32_e32 v5, v5, v45
	v_max_f32_e32 v17, 0, v17
	v_cvt_pk_bf16_f32 v14, v14, v15
	v_cvt_pk_bf16_f32 v15, v16, v17
	v_xor_b32_e32 v16, v18, v118
	v_max_f32_e32 v13, 0, v13
	v_cvt_pk_bf16_f32 v10, v10, v11
	v_cvt_pk_bf16_f32 v11, v12, v13
	v_bitop3_b32 v12, v18, v70, 31 bitop3:0x78
	v_max_f32_e32 v5, 0, v5
	v_cvt_pk_bf16_f32 v2, v2, v3
	v_cvt_pk_bf16_f32 v3, v4, v5
	v_bitop3_b32 v4, v18, v71, 31 bitop3:0x78
	v_lshlrev_b32_e32 v16, 4, v16
	v_lshlrev_b32_e32 v12, 4, v12
	v_add_f32_e32 v6, v6, v42
	v_add_f32_e32 v7, v7, v43
	v_lshlrev_b32_e32 v4, 4, v4
	v_add3_u32 v16, v69, v16, v68
	v_add3_u32 v12, v72, v12, v68
	v_max_f32_e32 v6, 0, v6
	v_max_f32_e32 v7, 0, v7
	v_add_f32_e32 v8, v8, v44
	v_add_f32_e32 v9, v9, v45
	v_add3_u32 v4, v73, v4, v68
	ds_write_b64 v16, v[14:15]
	ds_write_b64 v12, v[10:11]
	v_max_f32_e32 v8, 0, v8
	v_max_f32_e32 v9, 0, v9
	v_cvt_pk_bf16_f32 v6, v6, v7
	v_cvt_pk_bf16_f32 v7, v8, v9
	ds_write_b64 v16, v[6:7] offset:16384
	ds_write_b64 v4, v[2:3]
	v_and_b32_e32 v2, 0x1f0, v1
	v_mov_b32_e32 v3, 0
	v_lshl_add_u64 v[2:3], s[0:1], 0, v[2:3]
	s_mov_b64 s[0:1], 0x2000000
	v_ashrrev_i32_e32 v6, 5, v0
	v_lshl_add_u64 v[10:11], v[2:3], 0, s[0:1]
	v_xor_b32_e32 v2, v6, v0
	v_lshlrev_b32_e32 v2, 4, v2
	v_lshlrev_b32_e32 v1, 9, v6
	v_and_b32_e32 v2, 0x1f0, v2
	v_add3_u32 v1, 0, v1, v2
	s_waitcnt lgkmcnt(0)
	s_barrier
	ds_read_b128 v[2:5], v1
	v_ashrrev_i32_e32 v7, 31, v6
	v_add_u32_e32 v1, 0x200, v0
	v_lshlrev_b64 v[6:7], 11, v[6:7]
	v_ashrrev_i32_e32 v14, 5, v1
	v_lshl_add_u64 v[12:13], v[10:11], 0, v[6:7]
	v_xor_b32_e32 v6, v14, v0
	v_lshlrev_b32_e32 v6, 4, v6
	v_lshlrev_b32_e32 v1, 9, v14
	v_and_b32_e32 v6, 0x1f0, v6
	v_add3_u32 v1, 0, v1, v6
	ds_read_b128 v[6:9], v1
	v_ashrrev_i32_e32 v15, 31, v14
	s_waitcnt lgkmcnt(1)
	global_store_dwordx4 v[12:13], v[2:5], off sc1
	v_add_u32_e32 v1, 0x400, v0
	s_nop 0
	v_lshlrev_b64 v[2:3], 11, v[14:15]
	v_lshl_add_u64 v[2:3], v[10:11], 0, v[2:3]
	s_waitcnt lgkmcnt(0)
	global_store_dwordx4 v[2:3], v[6:9], off sc1
	s_nop 1
	v_ashrrev_i32_e32 v6, 5, v1
	v_xor_b32_e32 v2, v6, v0
	v_lshlrev_b32_e32 v2, 4, v2
	v_lshlrev_b32_e32 v1, 9, v6
	v_and_b32_e32 v2, 0x1f0, v2
	v_add3_u32 v1, 0, v1, v2
	ds_read_b128 v[2:5], v1
	v_ashrrev_i32_e32 v7, 31, v6
	v_add_u32_e32 v1, 0x600, v0
	v_lshlrev_b64 v[6:7], 11, v[6:7]
	v_ashrrev_i32_e32 v14, 5, v1
	v_lshl_add_u64 v[12:13], v[10:11], 0, v[6:7]
	v_xor_b32_e32 v6, v14, v0
	v_lshlrev_b32_e32 v6, 4, v6
	v_lshlrev_b32_e32 v1, 9, v14
	v_and_b32_e32 v6, 0x1f0, v6
	v_add3_u32 v1, 0, v1, v6
	ds_read_b128 v[6:9], v1
	v_ashrrev_i32_e32 v15, 31, v14
	s_waitcnt lgkmcnt(1)
	global_store_dwordx4 v[12:13], v[2:5], off sc1
	v_add_u32_e32 v1, 0x800, v0
	s_nop 0
	v_lshlrev_b64 v[2:3], 11, v[14:15]
	v_lshl_add_u64 v[2:3], v[10:11], 0, v[2:3]
	s_waitcnt lgkmcnt(0)
	global_store_dwordx4 v[2:3], v[6:9], off sc1
	s_nop 1
	v_ashrrev_i32_e32 v6, 5, v1
	v_xor_b32_e32 v2, v6, v0
	v_lshlrev_b32_e32 v2, 4, v2
	v_lshlrev_b32_e32 v1, 9, v6
	v_and_b32_e32 v2, 0x1f0, v2
	v_add3_u32 v1, 0, v1, v2
	ds_read_b128 v[2:5], v1
	v_ashrrev_i32_e32 v7, 31, v6
	v_add_u32_e32 v1, 0xa00, v0
	v_lshlrev_b64 v[6:7], 11, v[6:7]
	v_ashrrev_i32_e32 v14, 5, v1
	v_lshl_add_u64 v[12:13], v[10:11], 0, v[6:7]
	v_xor_b32_e32 v6, v14, v0
	v_lshlrev_b32_e32 v6, 4, v6
	v_lshlrev_b32_e32 v1, 9, v14
	v_and_b32_e32 v6, 0x1f0, v6
	v_add3_u32 v1, 0, v1, v6
	ds_read_b128 v[6:9], v1
	v_ashrrev_i32_e32 v15, 31, v14
	s_waitcnt lgkmcnt(1)
	global_store_dwordx4 v[12:13], v[2:5], off sc1
	v_add_u32_e32 v1, 0xc00, v0
	s_nop 0
	v_lshlrev_b64 v[2:3], 11, v[14:15]
	v_lshl_add_u64 v[2:3], v[10:11], 0, v[2:3]
	s_waitcnt lgkmcnt(0)
	global_store_dwordx4 v[2:3], v[6:9], off sc1
	s_nop 1
	v_ashrrev_i32_e32 v6, 5, v1
	v_xor_b32_e32 v2, v6, v0
	v_lshlrev_b32_e32 v2, 4, v2
	v_lshlrev_b32_e32 v1, 9, v6
	v_and_b32_e32 v2, 0x1f0, v2
	v_add3_u32 v1, 0, v1, v2
	ds_read_b128 v[2:5], v1
	v_add_u32_e32 v1, 0xe00, v0
	v_ashrrev_i32_e32 v14, 5, v1
	v_xor_b32_e32 v0, v14, v0
	v_lshlrev_b32_e32 v0, 4, v0
	v_ashrrev_i32_e32 v7, 31, v6
	v_lshlrev_b32_e32 v1, 9, v14
	v_and_b32_e32 v0, 0x1f0, v0
	v_lshlrev_b64 v[6:7], 11, v[6:7]
	v_add3_u32 v0, 0, v1, v0
	v_lshl_add_u64 v[12:13], v[10:11], 0, v[6:7]
	ds_read_b128 v[6:9], v0
	v_ashrrev_i32_e32 v15, 31, v14
	v_lshlrev_b64 v[0:1], 11, v[14:15]
	v_lshl_add_u64 v[0:1], v[10:11], 0, v[0:1]
	s_waitcnt lgkmcnt(1)
	global_store_dwordx4 v[12:13], v[2:5], off sc1
	s_waitcnt lgkmcnt(0)
	global_store_dwordx4 v[0:1], v[6:9], off sc1
	s_endpgm

.LBB2_2:
	s_or_b64 exec, exec, s[0:1]
	s_waitcnt lgkmcnt(0)
	ds_read_b128 v[36:39], v39
	ds_read_b128 v[44:47], v40
	ds_read_b128 v[48:51], v41
	ds_read_b128 v[40:43], v42
	v_or_b32_e32 v52, 0x3000, v34
	v_mov_b32_e32 v53, v35
	v_lshl_add_u64 v[52:53], v[32:33], 0, v[52:53]
	s_waitcnt lgkmcnt(3)
	global_store_dwordx4 v[52:53], v[36:39], off sc1
	s_add_u32 s26, s26, s34
	s_addc_u32 s27, s27, 0
	v_or_b32_e32 v36, 0x3400, v34
	v_mov_b32_e32 v37, v35
	v_lshl_add_u64 v[36:37], v[32:33], 0, v[36:37]
	s_waitcnt lgkmcnt(2)
	global_store_dwordx4 v[36:37], v[44:47], off sc1
	v_or_b32_e32 v36, 0x3800, v34
	v_mov_b32_e32 v37, v35
	v_or_b32_e32 v34, 0x3c00, v34
	v_lshl_add_u64 v[36:37], v[32:33], 0, v[36:37]
	v_lshl_add_u64 v[32:33], v[32:33], 0, v[34:35]
	s_waitcnt lgkmcnt(1)
	global_store_dwordx4 v[36:37], v[48:51], off sc1
	s_waitcnt lgkmcnt(0)
	global_store_dwordx4 v[32:33], v[40:43], off sc1
	s_waitcnt lgkmcnt(0)
	v_cmp_gt_u64_e32 vcc, s[26:27], v[202:203]
	s_cbranch_vccnz .LBB2_64

.LBB2_34:
	s_or_b64 exec, exec, s[4:5]
	v_lshrrev_b32_e32 v42, 4, v225
	s_lshl_b32 s4, s26, 11
	v_mov_b32_e32 v33, s29
	v_or_b32_e32 v32, s28, v200
	s_and_b32 s24, s4, 0x3800
	v_xor_b32_e32 v40, v42, v225
	v_lshl_add_u64 v[34:35], s[24:25], 0, v[32:33]
	v_lshlrev_b32_e32 v39, 8, v42
	v_lshlrev_b32_e32 v32, 4, v225
	v_lshlrev_b32_e32 v40, 4, v40
	v_and_or_b32 v200, v32, s80, v39
	v_add_u32_e32 v39, v214, v39
	v_and_b32_e32 v40, 0xf0, v40
	v_add_u32_e32 v39, v39, v40
	v_add_u32_e32 v40, 4, v42
	v_lshl_add_u32 v41, v40, 8, v214
	v_xor_b32_e32 v40, v40, v225
	v_lshlrev_b32_e32 v40, 4, v40
	v_and_b32_e32 v40, 0xf0, v40
	v_add_u32_e32 v40, v41, v40
	v_add_u32_e32 v41, 8, v42
	v_lshl_add_u32 v49, v41, 8, v214
	v_xor_b32_e32 v41, v41, v225
	s_waitcnt lgkmcnt(0)
	v_lshlrev_b32_e32 v41, 4, v41
	ds_read_b128 v[44:47], v39
	ds_read_b128 v[50:53], v40
	v_and_b32_e32 v41, 0xf0, v41
	v_add_u32_e32 v42, 12, v42
	v_add_u32_e32 v41, v49, v41
	v_lshl_add_u32 v49, v42, 8, v214
	v_xor_b32_e32 v42, v42, v225
	v_lshl_add_u64 v[32:33], s[14:15], 0, v[200:201]
	v_lshlrev_b32_e32 v42, 4, v42
	v_lshlrev_b64 v[34:35], 8, v[34:35]
	v_and_b32_e32 v42, 0xf0, v42
	v_lshl_add_u64 v[62:63], v[32:33], 0, v[34:35]
	v_add_u32_e32 v42, v49, v42
	ds_read_b128 v[54:57], v41
	ds_read_b128 v[58:61], v42
	s_waitcnt lgkmcnt(3)
	global_store_dwordx4 v[62:63], v[44:47], off sc1
	s_nop 1
	v_or_b32_e32 v44, 0x400, v34
	v_mov_b32_e32 v45, v35
	v_lshl_add_u64 v[44:45], v[32:33], 0, v[44:45]
	s_waitcnt lgkmcnt(2)
	global_store_dwordx4 v[44:45], v[50:53], off sc1
	v_or_b32_e32 v44, 0x800, v34
	v_mov_b32_e32 v45, v35
	v_lshl_add_u64 v[44:45], v[32:33], 0, v[44:45]
	s_waitcnt lgkmcnt(1)
	global_store_dwordx4 v[44:45], v[54:57], off sc1
	v_or_b32_e32 v44, 0xc00, v34
	v_mov_b32_e32 v45, v35
	v_lshl_add_u64 v[44:45], v[32:33], 0, v[44:45]
	s_waitcnt lgkmcnt(0)
	global_store_dwordx4 v[44:45], v[58:61], off sc1
	s_waitcnt lgkmcnt(0)
	s_nop 1
	v_accvgpr_read_b32 v60, a0
	v_accvgpr_read_b32 v59, a1
	v_accvgpr_read_b32 v58, a2
	v_accvgpr_read_b32 v57, a3
	v_accvgpr_read_b32 v56, a4
	v_accvgpr_read_b32 v55, a5
	v_accvgpr_read_b32 v54, a6
	v_accvgpr_read_b32 v53, a7
	v_accvgpr_read_b32 v52, a8
	v_accvgpr_read_b32 v51, a9
	v_accvgpr_read_b32 v50, a10
	v_accvgpr_read_b32 v49, a11
	v_accvgpr_read_b32 v47, a12
	v_accvgpr_read_b32 v46, a13
	v_accvgpr_read_b32 v45, a14
	v_accvgpr_read_b32 v44, a15

	s_and_saveexec_b64 s[4:5], vcc
	s_cbranch_execz .LBB2_36
	v_mul_f32_e32 v59, v59, v43
	v_mul_f32_e32 v57, v57, v43
	v_mul_f32_e32 v60, v60, v43
	v_mul_f32_e32 v61, v58, v43
	v_mul_f32_e32 v53, v53, v43
	v_mul_f32_e32 v54, v54, v43
	v_mul_f32_e32 v56, v56, v43
	v_mul_f32_e32 v49, v49, v43
	v_mul_f32_e32 v46, v46, v43
	v_mul_f32_e32 v45, v45, v43
	v_mul_f32_e32 v44, v44, v43
	v_mul_f32_e32 v50, v50, v43
	v_mul_f32_e32 v47, v47, v43
	v_mul_f32_e32 v52, v52, v43
	s_nop 0
	v_cvt_pk_f16_f32 v58, v60, v59
	v_cvt_pk_f16_f32 v59, v61, v57
	v_xad_u32 v57, v38, v37, v36
	ds_write_b64 v57, v[58:59]
	v_mul_f32_e32 v57, v55, v43
	v_cvt_pk_f16_f32 v55, v54, v53
	v_add_u32_e32 v53, 16, v38
	v_cvt_pk_f16_f32 v54, v56, v57
	v_xad_u32 v53, v53, v37, v36
	ds_write_b64 v53, v[54:55]
	v_mul_f32_e32 v53, v51, v43
	v_cvt_pk_f16_f32 v51, v50, v49
	v_add_u32_e32 v49, 32, v38
	v_cvt_pk_f16_f32 v45, v45, v44
	v_cvt_pk_f16_f32 v44, v47, v46
	v_add_u32_e32 v46, 48, v38
	v_cvt_pk_f16_f32 v50, v52, v53
	v_xad_u32 v49, v49, v37, v36
	v_xad_u32 v46, v46, v37, v36
	ds_write_b64 v49, v[50:51]
	ds_write_b64 v46, v[44:45]

.LBB2_42:
	s_or_b64 exec, exec, s[4:5]
	s_waitcnt lgkmcnt(0)
	ds_read_b128 v[44:47], v39
	ds_read_b128 v[50:53], v40
	ds_read_b128 v[54:57], v41
	ds_read_b128 v[58:61], v42
	v_or_b32_e32 v62, 0x1000, v34
	v_mov_b32_e32 v63, v35
	v_lshl_add_u64 v[62:63], v[32:33], 0, v[62:63]
	s_waitcnt lgkmcnt(3)
	global_store_dwordx4 v[62:63], v[44:47], off sc1
	v_rcp_f32_e32 v43, v48
	v_cmp_lt_f32_e64 s[4:5], 0, v48
	v_or_b32_e32 v44, 0x1400, v34
	v_mov_b32_e32 v45, v35
	v_lshl_add_u64 v[44:45], v[32:33], 0, v[44:45]
	s_waitcnt lgkmcnt(2)
	global_store_dwordx4 v[44:45], v[50:53], off sc1
	v_or_b32_e32 v44, 0x1800, v34
	v_mov_b32_e32 v45, v35
	v_lshl_add_u64 v[44:45], v[32:33], 0, v[44:45]
	s_waitcnt lgkmcnt(1)
	global_store_dwordx4 v[44:45], v[54:57], off sc1
	v_or_b32_e32 v44, 0x1c00, v34
	v_mov_b32_e32 v45, v35
	v_lshl_add_u64 v[44:45], v[32:33], 0, v[44:45]
	s_waitcnt lgkmcnt(0)
	global_store_dwordx4 v[44:45], v[58:61], off sc1
	s_waitcnt lgkmcnt(0)
	v_cndmask_b32_e64 v43, 0, v43, s[4:5]
	s_nop 0
	v_accvgpr_read_b32 v59, a16
	v_accvgpr_read_b32 v58, a17
	v_accvgpr_read_b32 v57, a18
	v_accvgpr_read_b32 v56, a19
	v_accvgpr_read_b32 v55, a20
	v_accvgpr_read_b32 v54, a21
	v_accvgpr_read_b32 v53, a22
	v_accvgpr_read_b32 v52, a23
	v_accvgpr_read_b32 v51, a24
	v_accvgpr_read_b32 v50, a25
	v_accvgpr_read_b32 v49, a26
	v_accvgpr_read_b32 v48, a27
	v_accvgpr_read_b32 v47, a28
	v_accvgpr_read_b32 v46, a29
	v_accvgpr_read_b32 v45, a30
	v_accvgpr_read_b32 v44, a31

	s_and_saveexec_b64 s[4:5], s[0:1]
	s_cbranch_execz .LBB2_44
	v_mul_f32_e32 v54, v54, v43
	v_mul_f32_e32 v53, v53, v43
	v_mul_f32_e32 v52, v52, v43
	v_mul_f32_e32 v50, v50, v43
	v_mul_f32_e32 v49, v49, v43
	v_mul_f32_e32 v48, v48, v43
	v_mul_f32_e32 v46, v46, v43
	v_mul_f32_e32 v45, v45, v43
	v_mul_f32_e32 v44, v44, v43
	v_mul_f32_e32 v58, v58, v43
	v_mul_f32_e32 v57, v57, v43
	v_mul_f32_e32 v55, v55, v43
	v_mul_f32_e32 v51, v51, v43
	v_mul_f32_e32 v47, v47, v43
	v_mul_f32_e32 v59, v59, v43
	v_mul_f32_e32 v60, v56, v43
	s_nop 0
	v_cvt_pk_f16_f32 v53, v53, v52
	v_cvt_pk_f16_f32 v52, v55, v54
	v_add_u32_e32 v54, 16, v38
	v_cvt_pk_f16_f32 v49, v49, v48
	v_cvt_pk_f16_f32 v48, v51, v50
	v_add_u32_e32 v50, 32, v38
	v_cvt_pk_f16_f32 v45, v45, v44
	v_cvt_pk_f16_f32 v44, v47, v46
	v_add_u32_e32 v46, 48, v38
	v_cvt_pk_f16_f32 v56, v59, v58
	v_cvt_pk_f16_f32 v57, v57, v60
	v_xad_u32 v58, v38, v37, v36
	v_xad_u32 v54, v54, v37, v36
	v_xad_u32 v50, v50, v37, v36
	v_xad_u32 v46, v46, v37, v36
	ds_write_b64 v58, v[56:57]
	ds_write_b64 v54, v[52:53]
	ds_write_b64 v50, v[48:49]
	ds_write_b64 v46, v[44:45]

.LBB2_50:
	s_or_b64 exec, exec, s[4:5]
	s_waitcnt lgkmcnt(0)
	ds_read_b128 v[44:47], v39
	ds_read_b128 v[48:51], v40
	ds_read_b128 v[52:55], v41
	ds_read_b128 v[56:59], v42
	v_or_b32_e32 v60, 0x2000, v34
	v_mov_b32_e32 v61, v35
	v_lshl_add_u64 v[60:61], v[32:33], 0, v[60:61]
	s_waitcnt lgkmcnt(3)
	global_store_dwordx4 v[60:61], v[44:47], off sc1
	s_nop 1
	v_or_b32_e32 v44, 0x2400, v34
	v_mov_b32_e32 v45, v35
	v_lshl_add_u64 v[44:45], v[32:33], 0, v[44:45]
	s_waitcnt lgkmcnt(2)
	global_store_dwordx4 v[44:45], v[48:51], off sc1
	v_or_b32_e32 v44, 0x2800, v34
	v_mov_b32_e32 v45, v35
	v_lshl_add_u64 v[44:45], v[32:33], 0, v[44:45]
	s_waitcnt lgkmcnt(1)
	global_store_dwordx4 v[44:45], v[52:55], off sc1
	v_or_b32_e32 v44, 0x2c00, v34
	v_mov_b32_e32 v45, v35
	v_lshl_add_u64 v[44:45], v[32:33], 0, v[44:45]
	s_waitcnt lgkmcnt(0)
	global_store_dwordx4 v[44:45], v[56:59], off sc1
	s_waitcnt lgkmcnt(0)
	s_nop 1
	v_accvgpr_read_b32 v59, a16
	v_accvgpr_read_b32 v58, a17
	v_accvgpr_read_b32 v57, a18
	v_accvgpr_read_b32 v56, a19
	v_accvgpr_read_b32 v55, a20
	v_accvgpr_read_b32 v54, a21
	v_accvgpr_read_b32 v53, a22
	v_accvgpr_read_b32 v52, a23
	v_accvgpr_read_b32 v51, a24
	v_accvgpr_read_b32 v50, a25
	v_accvgpr_read_b32 v49, a26
	v_accvgpr_read_b32 v48, a27
	v_accvgpr_read_b32 v47, a28
	v_accvgpr_read_b32 v46, a29
	v_accvgpr_read_b32 v45, a30
	v_accvgpr_read_b32 v44, a31

	s_and_saveexec_b64 s[0:1], vcc
	s_cbranch_execz .LBB2_52
	v_mul_f32_e32 v54, v54, v43
	v_mul_f32_e32 v53, v53, v43
	v_mul_f32_e32 v52, v52, v43
	v_mul_f32_e32 v50, v50, v43
	v_mul_f32_e32 v49, v49, v43
	v_mul_f32_e32 v48, v48, v43
	v_mul_f32_e32 v46, v46, v43
	v_mul_f32_e32 v45, v45, v43
	v_mul_f32_e32 v44, v44, v43
	v_mul_f32_e32 v58, v58, v43
	v_mul_f32_e32 v57, v57, v43
	v_mul_f32_e32 v55, v55, v43
	v_mul_f32_e32 v51, v51, v43
	v_mul_f32_e32 v47, v47, v43
	v_mul_f32_e32 v59, v59, v43
	v_mul_f32_e32 v60, v56, v43
	s_nop 0
	v_cvt_pk_f16_f32 v53, v53, v52
	v_cvt_pk_f16_f32 v52, v55, v54
	v_add_u32_e32 v54, 16, v38
	v_cvt_pk_f16_f32 v49, v49, v48
	v_cvt_pk_f16_f32 v48, v51, v50
	v_add_u32_e32 v50, 32, v38
	v_cvt_pk_f16_f32 v45, v45, v44
	v_cvt_pk_f16_f32 v44, v47, v46
	v_add_u32_e32 v46, 48, v38
	v_cvt_pk_f16_f32 v56, v59, v58
	v_cvt_pk_f16_f32 v57, v57, v60
	v_xad_u32 v58, v38, v37, v36
	v_xad_u32 v54, v54, v37, v36
	v_xad_u32 v50, v50, v37, v36
	v_xad_u32 v46, v46, v37, v36
	ds_write_b64 v58, v[56:57]
	ds_write_b64 v54, v[52:53]
	ds_write_b64 v50, v[48:49]
	ds_write_b64 v46, v[44:45]

_Z8out_projPKDF16_S0_PKfPf:
	s_load_dwordx8 s[4:11], s[0:1], 0x0
	s_lshl_b32 s1, s2, 5
	s_lshr_b32 s0, s2, 6
	s_and_b32 s3, s1, 0x7e0
	s_mov_b32 s1, 0
	v_lshrrev_b32_e32 v92, 6, v0
	s_lshl_b64 s[12:13], s[0:1], 14
	v_lshl_or_b32 v2, v92, 11, s12
	v_or_b32_e32 v2, s3, v2
	v_mov_b32_e32 v3, s13
	v_and_b32_e32 v1, 63, v0
	v_lshlrev_b64 v[2:3], 8, v[2:3]
	v_lshlrev_b32_e32 v64, 15, v92
	v_mov_b32_e32 v65, 0
	s_waitcnt lgkmcnt(0)
	v_lshl_add_u64 v[2:3], s[4:5], 0, v[2:3]
	v_lshl_add_u64 v[34:35], s[6:7], 0, v[64:65]
	v_lshlrev_b32_e32 v64, 4, v1
	v_lshl_add_u64 v[18:19], v[2:3], 0, v[64:65]
	s_movk_i32 s4, 0x1000
	v_add_co_u32_e32 v36, vcc, s4, v18
	global_load_dwordx4 v[2:5], v[18:19], off
	global_load_dwordx4 v[6:9], v[18:19], off offset:1024
	v_addc_co_u32_e32 v37, vcc, 0, v19, vcc
	global_load_dwordx4 v[10:13], v[18:19], off offset:3072
	global_load_dwordx4 v[14:17], v[18:19], off offset:2048
	s_nop 0
	global_load_dwordx4 v[18:21], v[36:37], off
	global_load_dwordx4 v[22:25], v[36:37], off offset:1024
	global_load_dwordx4 v[26:29], v[36:37], off offset:2048
	global_load_dwordx4 v[30:33], v[36:37], off offset:3072
	s_lshl_b32 s4, s2, 9
	s_mov_b32 s5, s1
	s_and_b32 s4, s4, 0x7000
	v_lshl_add_u64 v[66:67], v[34:35], 0, v[64:65]
	v_lshl_add_u64 v[46:47], v[66:67], 0, s[4:5]
	global_load_dwordx4 v[34:37], v[46:47], off
	s_lshr_b32 s4, s2, 3
	s_add_i32 s5, s4, 1
	s_lshl_b32 s6, s5, 12
	s_mov_b32 s7, s1
	s_and_b32 s6, s6, 0x7000
	v_lshl_add_u64 v[72:73], v[66:67], 0, s[6:7]
	global_load_dwordx4 v[38:41], v[72:73], off
	global_load_dwordx4 v[42:45], v[46:47], off offset:1024
	global_load_dwordx4 v[48:51], v[72:73], off offset:1024
	global_load_dwordx4 v[52:55], v[46:47], off offset:2048
	v_or_b32_e32 v60, 64, v1
	v_or_b32_e32 v61, 0xc0, v1
	v_or_b32_e32 v62, 0x140, v1
	v_or_b32_e32 v1, 0x1c0, v1
	v_lshlrev_b32_e32 v56, 4, v60
	v_lshlrev_b32_e32 v57, 4, v61
	v_lshlrev_b32_e32 v58, 4, v62
	v_lshlrev_b32_e32 v59, 4, v1
	v_lshlrev_b32_e32 v64, 4, v0
	s_movk_i32 s6, 0x70
	v_and_b32_e32 v75, 0x700, v56
	v_and_b32_e32 v76, 0xf00, v57
	v_and_b32_e32 v77, 0x1700, v58
	v_and_b32_e32 v78, 0x1f00, v59
	v_and_b32_e32 v63, 0xf0, v64
	global_load_dwordx4 v[56:59], v[72:73], off offset:2048
	v_and_b32_e32 v93, 31, v0
	v_bfe_u32 v94, v0, 5, 1
	v_bitop3_b32 v0, v0, v63, 48 bitop3:0x6c
	v_bitop3_b32 v80, v60, v63, s6 bitop3:0x6c
	v_bitop3_b32 v81, v61, v63, s6 bitop3:0x6c
	v_bitop3_b32 v82, v62, v63, s6 bitop3:0x6c
	v_bitop3_b32 v1, v1, v63, s6 bitop3:0x6c
	global_load_dwordx4 v[60:63], v[46:47], off offset:3072
	global_load_dwordx4 v[68:71], v[72:73], off offset:3072
	v_lshl_add_u32 v74, v92, 13, 0
	v_and_b32_e32 v79, 0x300, v64
	s_lshl_b32 s6, s2, 2
	v_add3_u32 v0, v74, v79, v0
	v_lshlrev_b32_e32 v86, 4, v94
	s_and_b32 s6, s6, 0xe0
	v_add3_u32 v46, v74, v75, v80
	v_add3_u32 v47, v74, v76, v81
	v_add3_u32 v72, v74, v77, v82
	v_add3_u32 v1, v74, v78, v1
	v_and_b32_e32 v87, 0x70, v64
	v_lshl_add_u32 v95, v93, 8, v74
	s_lshl_b32 s5, s5, 5
	s_and_b32 s5, s5, 0xe0
	s_bfe_u32 s2, s2, 0x30003
	s_xor_b32 s2, s2, 4
	s_waitcnt vmcnt(15)
	ds_write_b128 v0, v[2:5]
	s_waitcnt vmcnt(14)
	ds_write_b128 v46, v[6:9]
	s_waitcnt vmcnt(13)
	ds_write_b128 v47, v[10:13]
	s_waitcnt vmcnt(12)
	ds_write_b128 v0, v[14:17] offset:2048
	s_waitcnt vmcnt(11)
	ds_write_b128 v0, v[18:21] offset:4096
	s_waitcnt vmcnt(10)
	ds_write_b128 v72, v[22:25]
	s_waitcnt vmcnt(9)
	ds_write_b128 v0, v[26:29] offset:6144
	s_waitcnt vmcnt(8)
	ds_write_b128 v1, v[30:33]
	v_or_b32_e32 v0, s6, v86
	v_xad_u32 v0, v0, v87, v95
	s_waitcnt lgkmcnt(0)
	s_barrier
	ds_read_b128 v[72:75], v0
	v_or_b32_e32 v0, s5, v86
	v_xad_u32 v0, v0, v87, v95
	ds_read_b128 v[76:79], v0
	s_waitcnt vmcnt(7) lgkmcnt(1)
	v_mfma_f32_32x32x16_f16 v[16:31], v[72:75], v[34:37], 0
	s_add_i32 s5, s4, 2
	s_and_b32 s5, s5, 7
	s_lshl_b32 s6, s5, 12
	v_lshl_add_u64 v[84:85], v[66:67], 0, s[6:7]
	global_load_dwordx4 v[80:83], v[84:85], off
	s_waitcnt vmcnt(7) lgkmcnt(0)
	v_mfma_f32_32x32x16_f16 v[16:31], v[76:79], v[38:41], v[16:31]
	s_waitcnt vmcnt(6)
	v_mfma_f32_32x32x16_f16 v[32:47], v[72:75], v[42:45], 0
	s_waitcnt vmcnt(4)
	v_mfma_f32_32x32x16_f16 v[0:15], v[72:75], v[52:55], 0
	v_mfma_f32_32x32x16_f16 v[32:47], v[76:79], v[48:51], v[32:47]
	s_waitcnt vmcnt(3)
	v_mfma_f32_32x32x16_f16 v[0:15], v[76:79], v[56:59], v[0:15]
	s_waitcnt vmcnt(2)
	v_mfma_f32_32x32x16_f16 v[48:63], v[72:75], v[60:63], 0
	global_load_dwordx4 v[72:75], v[84:85], off offset:1024
	s_waitcnt vmcnt(2)
	v_mfma_f32_32x32x16_f16 v[48:63], v[76:79], v[68:71], v[48:63]
	global_load_dwordx4 v[68:71], v[84:85], off offset:2048
	v_lshl_or_b32 v76, s5, 5, v86
	v_xad_u32 v76, v76, v87, v95
	ds_read_b128 v[76:79], v76
	s_add_i32 s5, s4, 3
	s_and_b32 s5, s5, 7
	s_lshl_b32 s6, s5, 12
	s_waitcnt vmcnt(2) lgkmcnt(0)
	v_mfma_f32_32x32x16_f16 v[16:31], v[76:79], v[80:83], v[16:31]
	global_load_dwordx4 v[80:83], v[84:85], off offset:3072
	v_lshl_add_u64 v[84:85], v[66:67], 0, s[6:7]
	s_lshl_b32 s6, s2, 12
	s_waitcnt vmcnt(2)
	v_mfma_f32_32x32x16_f16 v[32:47], v[76:79], v[72:75], v[32:47]
	global_load_dwordx4 v[72:75], v[84:85], off
	s_waitcnt vmcnt(2)
	v_mfma_f32_32x32x16_f16 v[0:15], v[76:79], v[68:71], v[0:15]
	global_load_dwordx4 v[68:71], v[84:85], off offset:1024
	s_waitcnt vmcnt(2)
	v_mfma_f32_32x32x16_f16 v[48:63], v[76:79], v[80:83], v[48:63]
	global_load_dwordx4 v[76:79], v[84:85], off offset:2048
	v_lshl_or_b32 v80, s5, 5, v86
	v_xad_u32 v80, v80, v87, v95
	ds_read_b128 v[80:83], v80
	s_mov_b32 s5, s1
	s_lshl_b64 s[0:1], s[0:1], 20
	s_waitcnt vmcnt(2) lgkmcnt(0)
	v_mfma_f32_32x32x16_f16 v[16:31], v[80:83], v[72:75], v[16:31]
	global_load_dwordx4 v[72:75], v[84:85], off offset:3072
	v_lshl_add_u64 v[84:85], v[66:67], 0, s[6:7]
	s_waitcnt vmcnt(2)
	v_mfma_f32_32x32x16_f16 v[32:47], v[80:83], v[68:71], v[32:47]
	global_load_dwordx4 v[68:71], v[84:85], off
	s_waitcnt vmcnt(2)
	v_mfma_f32_32x32x16_f16 v[0:15], v[80:83], v[76:79], v[0:15]
	global_load_dwordx4 v[76:79], v[84:85], off offset:1024
	s_waitcnt vmcnt(2)
	v_mfma_f32_32x32x16_f16 v[48:63], v[80:83], v[72:75], v[48:63]
	global_load_dwordx4 v[72:75], v[84:85], off offset:2048
	v_lshl_or_b32 v80, s2, 5, v86
	v_xad_u32 v80, v80, v87, v95
	ds_read_b128 v[80:83], v80
	s_add_i32 s2, s4, 5
	s_and_b32 s2, s2, 7
	s_lshl_b32 s6, s2, 12
	s_waitcnt vmcnt(2) lgkmcnt(0)
	v_mfma_f32_32x32x16_f16 v[16:31], v[80:83], v[68:71], v[16:31]
	global_load_dwordx4 v[68:71], v[84:85], off offset:3072
	v_lshl_add_u64 v[84:85], v[66:67], 0, s[6:7]
	s_waitcnt vmcnt(2)
	v_mfma_f32_32x32x16_f16 v[32:47], v[80:83], v[76:79], v[32:47]
	global_load_dwordx4 v[76:79], v[84:85], off
	s_waitcnt vmcnt(2)
	v_mfma_f32_32x32x16_f16 v[0:15], v[80:83], v[72:75], v[0:15]
	global_load_dwordx4 v[72:75], v[84:85], off offset:1024
	s_waitcnt vmcnt(2)
	v_mfma_f32_32x32x16_f16 v[48:63], v[80:83], v[68:71], v[48:63]
	v_lshl_or_b32 v68, s2, 5, v86
	v_xad_u32 v68, v68, v87, v95
	ds_read_b128 v[68:71], v68
	global_load_dwordx4 v[80:83], v[84:85], off offset:2048
	s_add_i32 s2, s4, 6
	s_and_b32 s2, s2, 7
	s_lshl_b32 s6, s2, 12
	s_waitcnt vmcnt(2) lgkmcnt(0)
	v_mfma_f32_32x32x16_f16 v[16:31], v[68:71], v[76:79], v[16:31]
	global_load_dwordx4 v[76:79], v[84:85], off offset:3072
	v_lshl_add_u64 v[88:89], v[66:67], 0, s[6:7]
	s_add_i32 s4, s4, -1
	s_and_b32 s6, s4, 7
	s_lshl_b32 s4, s6, 12
	v_lshl_add_u64 v[90:91], v[66:67], 0, s[4:5]
	s_add_u32 s0, s10, s0
	s_waitcnt vmcnt(2)
	v_mfma_f32_32x32x16_f16 v[32:47], v[68:71], v[72:75], v[32:47]
	global_load_dwordx4 v[72:75], v[88:89], off
	s_addc_u32 s1, s11, s1
	s_waitcnt vmcnt(2)
	v_mfma_f32_32x32x16_f16 v[0:15], v[68:71], v[80:83], v[0:15]
	global_load_dwordx4 v[80:83], v[88:89], off offset:1024
	s_waitcnt vmcnt(2)
	v_mfma_f32_32x32x16_f16 v[48:63], v[68:71], v[76:79], v[48:63]
	v_lshl_or_b32 v70, s2, 5, v86
	v_xad_u32 v70, v70, v87, v95
	ds_read_b128 v[76:79], v70
	global_load_dwordx4 v[66:69], v[90:91], off
	s_lshl_b32 s2, s3, 9
	s_add_u32 s0, s0, s2
	s_addc_u32 s1, s1, 0
	s_waitcnt vmcnt(2) lgkmcnt(0)
	v_mfma_f32_32x32x16_f16 v[16:31], v[76:79], v[72:75], v[16:31]
	global_load_dwordx4 v[70:73], v[90:91], off offset:1024
	v_lshl_or_b32 v74, s6, 5, v86
	v_xad_u32 v74, v74, v87, v95
	v_lshlrev_b32_e32 v75, 11, v94
	s_waitcnt vmcnt(2)
	v_mfma_f32_32x32x16_f16 v[32:47], v[76:79], v[80:83], v[32:47]
	ds_read_b128 v[80:83], v74
	v_lshl_add_u32 v74, v92, 14, 0
	s_waitcnt vmcnt(1) lgkmcnt(0)
	v_mfma_f32_32x32x16_f16 v[16:31], v[80:83], v[66:69], v[16:31]
	global_load_dwordx4 v[66:69], v[88:89], off offset:2048
	global_load_dwordx4 v[84:87], v[88:89], off offset:3072
	v_lshlrev_b32_e32 v88, 2, v93
	v_add3_u32 v74, v74, v75, v88
	s_waitcnt vmcnt(2)
	v_mfma_f32_32x32x16_f16 v[32:47], v[80:83], v[70:73], v[32:47]
	global_load_dwordx4 v[70:73], v[90:91], off offset:2048
	s_nop 0
	global_load_dwordx4 v[88:91], v[90:91], off offset:3072
	s_barrier
	s_nop 7
	ds_write2_b32 v74, v16, v32 offset1:32
	ds_write2_b32 v74, v17, v33 offset0:128 offset1:160
	s_waitcnt vmcnt(3)
	v_mfma_f32_32x32x16_f16 v[0:15], v[76:79], v[66:69], v[0:15]
	v_add_u32_e32 v16, 0x400, v74
	ds_write2_b32 v16, v18, v34 offset1:32
	ds_write2_b32 v16, v19, v35 offset0:128 offset1:160
	v_add_u32_e32 v17, 0x1000, v74
	v_add_u32_e32 v18, 0x1400, v74
	ds_write2_b32 v17, v20, v36 offset1:32
	ds_write2_b32 v17, v21, v37 offset0:128 offset1:160
	ds_write2_b32 v18, v22, v38 offset1:32
	ds_write2_b32 v18, v23, v39 offset0:128 offset1:160
	v_add_u32_e32 v19, 0x2000, v74
	s_waitcnt vmcnt(2)
	v_mfma_f32_32x32x16_f16 v[48:63], v[76:79], v[84:87], v[48:63]
	v_add_u32_e32 v20, 0x2400, v74
	v_add_u32_e32 v21, 0x3000, v74
	v_add_u32_e32 v22, 0x3400, v74
	ds_write2_b32 v19, v24, v40 offset1:32
	ds_write2_b32 v19, v25, v41 offset0:128 offset1:160
	ds_write2_b32 v20, v26, v42 offset1:32
	ds_write2_b32 v20, v27, v43 offset0:128 offset1:160
	ds_write2_b32 v21, v28, v44 offset1:32
	ds_write2_b32 v21, v29, v45 offset0:128 offset1:160
	s_waitcnt vmcnt(1)
	v_mfma_f32_32x32x16_f16 v[0:15], v[80:83], v[70:73], v[0:15]
	ds_write2_b32 v22, v30, v46 offset1:32
	ds_write2_b32 v22, v31, v47 offset0:128 offset1:160
	s_waitcnt vmcnt(0)
	v_mfma_f32_32x32x16_f16 v[48:63], v[80:83], v[88:91], v[48:63]
	s_nop 11
	ds_write2_b32 v74, v0, v48 offset0:64 offset1:96
	ds_write2_b32 v74, v1, v49 offset0:192 offset1:224
	ds_write2_b32 v16, v2, v50 offset0:64 offset1:96
	ds_write2_b32 v16, v3, v51 offset0:192 offset1:224
	ds_write2_b32 v17, v4, v52 offset0:64 offset1:96
	ds_write2_b32 v17, v5, v53 offset0:192 offset1:224
	ds_write2_b32 v18, v6, v54 offset0:64 offset1:96
	ds_write2_b32 v18, v7, v55 offset0:192 offset1:224
	ds_write2_b32 v19, v8, v56 offset0:64 offset1:96
	ds_write2_b32 v19, v9, v57 offset0:192 offset1:224
	ds_write2_b32 v20, v10, v58 offset0:64 offset1:96
	ds_write2_b32 v20, v11, v59 offset0:192 offset1:224
	ds_write2_b32 v21, v12, v60 offset0:64 offset1:96
	ds_write2_b32 v21, v13, v61 offset0:192 offset1:224
	ds_write2_b32 v22, v14, v62 offset0:64 offset1:96
	ds_write2_b32 v22, v15, v63 offset0:192 offset1:224
	v_and_b32_e32 v0, 0x1f0, v64
	s_waitcnt lgkmcnt(0)
	s_barrier
	global_load_dwordx4 v[0:3], v0, s[8:9]
	v_add_u32_e32 v54, 0, v64
	v_add_u32_e32 v4, 0x10000, v54
	v_add_u32_e32 v8, 0x14000, v54
	v_add_u32_e32 v12, 0x18000, v54
	v_add_u32_e32 v16, 0x1c000, v54
	ds_read_b128 v[4:7], v4
	ds_read_b128 v[8:11], v8
	ds_read_b128 v[12:15], v12
	ds_read_b128 v[16:19], v16
	ds_read_b128 v[20:23], v54
	ds_read_b128 v[24:27], v54 offset:8192
	ds_read_b128 v[28:31], v54 offset:16384
	ds_read_b128 v[32:35], v54 offset:24576
	ds_read_b128 v[36:39], v54 offset:32768
	ds_read_b128 v[40:43], v54 offset:40960
	ds_read_b128 v[44:47], v54 offset:49152
	ds_read_b128 v[48:51], v54 offset:57344
	v_lshl_add_u64 v[52:53], s[0:1], 0, v[64:65]
	s_waitcnt vmcnt(0) lgkmcnt(7)
	v_pk_add_f32 v[22:23], v[2:3], v[22:23]
	v_pk_add_f32 v[20:21], v[0:1], v[20:21]
	s_waitcnt lgkmcnt(6)
	v_pk_add_f32 v[2:3], v[2:3], v[26:27]
	v_pk_add_f32 v[0:1], v[0:1], v[24:25]
	s_waitcnt lgkmcnt(5)
	v_pk_add_f32 v[22:23], v[22:23], v[30:31]
	v_pk_add_f32 v[20:21], v[20:21], v[28:29]
	s_waitcnt lgkmcnt(4)
	v_pk_add_f32 v[2:3], v[2:3], v[34:35]
	v_pk_add_f32 v[24:25], v[0:1], v[32:33]
	s_waitcnt lgkmcnt(3)
	v_pk_add_f32 v[0:1], v[22:23], v[38:39]
	v_pk_add_f32 v[20:21], v[20:21], v[36:37]
	s_waitcnt lgkmcnt(2)
	v_pk_add_f32 v[22:23], v[2:3], v[42:43]
	s_waitcnt lgkmcnt(1)
	v_pk_add_f32 v[0:1], v[0:1], v[46:47]
	v_pk_add_f32 v[2:3], v[20:21], v[44:45]
	v_pk_add_f32 v[0:1], v[0:1], v[6:7]
	v_pk_add_f32 v[2:3], v[2:3], v[4:5]
	v_pk_add_f32 v[0:1], v[0:1], v[10:11]
	v_pk_add_f32 v[2:3], v[2:3], v[8:9]
	v_pk_add_f32 v[0:1], v[0:1], v[14:15]
	v_pk_add_f32 v[4:5], v[2:3], v[12:13]
	v_pk_add_f32 v[2:3], v[0:1], v[18:19]
	v_pk_add_f32 v[0:1], v[4:5], v[16:17]
	global_store_dwordx4 v64, v[0:3], s[0:1] sc1
	v_pk_add_f32 v[4:5], v[24:25], v[40:41]
	s_waitcnt lgkmcnt(0)
	v_pk_add_f32 v[8:9], v[22:23], v[50:51]
	v_add_u32_e32 v0, 0x12000, v54
	ds_read_b128 v[0:3], v0
	v_pk_add_f32 v[10:11], v[4:5], v[48:49]
	v_add_u32_e32 v4, 0x16000, v54
	ds_read_b128 v[4:7], v4
	s_waitcnt lgkmcnt(1)
	v_pk_add_f32 v[14:15], v[10:11], v[0:1]
	v_add_u32_e32 v0, 0x1a000, v54
	v_pk_add_f32 v[12:13], v[8:9], v[2:3]
	ds_read_b128 v[0:3], v0
	v_add_u32_e32 v8, 0x1e000, v54
	ds_read_b128 v[8:11], v8
	s_waitcnt lgkmcnt(2)
	v_pk_add_f32 v[6:7], v[12:13], v[6:7]
	v_pk_add_f32 v[4:5], v[14:15], v[4:5]
	s_waitcnt lgkmcnt(1)
	v_pk_add_f32 v[2:3], v[6:7], v[2:3]
	v_pk_add_f32 v[0:1], v[4:5], v[0:1]
	v_add_co_u32_e32 v4, vcc, 0x2000, v52
	s_waitcnt lgkmcnt(0)
	v_pk_add_f32 v[2:3], v[2:3], v[10:11]
	v_pk_add_f32 v[0:1], v[0:1], v[8:9]
	v_addc_co_u32_e32 v5, vcc, 0, v53, vcc
	global_store_dwordx4 v[4:5], v[0:3], off sc1
	s_endpgm
